# router top-4: logits read once into registers and selected with register scans instead of 128 serialized LDS reads
# speedup vs baseline: 1.0065x; 1.0005x over previous
; #define GAS __attribute__((address_space(1)))
; #define LAS __attribute__((address_space(3)))
; __device__ __forceinline__ unsigned cvt_pk_bf16(float lo, float hi) { unsigned r; asm volatile("v_cvt_pk_bf16_f32 %0, %1, %2" : "=v"(r) : "v"(lo), "v"(hi)); return r; }
; #define FLANE lane_id()
; __device__ __forceinline__ void p6_router(Frame& F) {
;     ...
;         for (int kc = 0; kc < 8; ++kc) {
;             { const int ln = FLANE, col = kc * 256 + ln * 4; const f32x4 g = *(const GAS f32x4*)(F.ln1_g + col), b = *(const GAS f32x4*)(F.ln1_b + col);
; #pragma unroll
;               for (int i = 0; i < 8; ++i) { const int r = F.wave + 8 * i; const v2u zw = zp[i];
;                 const f32x4 zv = (f32x4){bf_lo(zw.x), bf_hi(zw.x), bf_lo(zw.y), bf_hi(zw.y)};
;                 const f32x4 hh = (zv - stl[2 * r]) * stl[2 * r + 1] * g + b;
;                 v2u hi, lo; hi.x = cvt_pk_bf16(hh[0], hh[1]); hi.y = cvt_pk_bf16(hh[2], hh[3]);
;                 lo.x = cvt_pk_bf16(hh[0] - bf_lo(hi.x), hh[1] - bf_hi(hi.x)); lo.y = cvt_pk_bf16(hh[2] - bf_lo(hi.y), hh[3] - bf_hi(hi.y));
;                 *(LAS v2u*)(Hhi + r * HP + ln * 8) = hi; *(LAS v2u*)(Hlo + r * HP + ln * 8) = lo; }
; #pragma unroll
;               for (int i = 0; i < 4; ++i) { const int q = F.wave * 64 + ln + NTHR * i, e = (q >> 5) & 31, c8 = q & 31; *(LAS v4u*)(((q >> 10) ? Wlo : Whi) + e * HP + c8 * 16) = wp[i]; } }
.LBB0_1500:
	v_mbcnt_lo_u32_b32 v32, -1, 0
	v_mbcnt_hi_u32_b32 v32, -1, v32
	s_add_i32 s46, 0, 0x18c00
	v_lshl_add_u32 v24, v32, 2, s40
	v_ashrrev_i32_e32 v25, 31, v24
	v_lshlrev_b64 v[28:29], 2, v[24:25]
	v_lshl_add_u64 v[24:25], s[12:13], 0, v[28:29]
	v_lshl_add_u64 v[28:29], s[14:15], 0, v[28:29]
	global_load_dwordx4 v[24:27], v[24:25], off
	s_add_i32 s67, s46, s65
	global_load_dwordx4 v[28:31], v[28:29], off
	s_waitcnt vmcnt(13)
	v_lshlrev_b32_e32 v54, 16, v50
	v_and_b32_e32 v55, 0xffff0000, v50
	v_mov_b32_e32 v50, s67
	v_lshlrev_b32_e32 v52, 16, v51
	v_and_b32_e32 v53, 0xffff0000, v51
	ds_read_b64 v[50:51], v50
	s_add_i32 s69, s46, s91
	s_add_i32 s41, s46, s92
	s_add_i32 s47, s46, s93
	s_add_i32 s9, s46, s94
	s_waitcnt lgkmcnt(0)
	v_sub_f32_e32 v55, v55, v50
	v_sub_f32_e32 v54, v54, v50
	v_sub_f32_e32 v53, v53, v50
	v_sub_f32_e32 v52, v52, v50
	v_pk_mul_f32 v[54:55], v[50:51], v[54:55] op_sel:[1,0]
	v_pk_mul_f32 v[50:51], v[50:51], v[52:53] op_sel:[1,0]
	s_add_i32 s0, s46, s95
	s_add_i32 s51, s46, s96
	s_add_i32 s46, s46, s97
	s_add_u32 s6, s28, s2
	s_addc_u32 s7, s29, s8
	s_waitcnt vmcnt(0)
	v_pk_fma_f32 v[52:53], v[24:25], v[54:55], v[28:29]
	s_nop 0
	v_cvt_pk_bf16_f32 v54, v52, v53
	v_pk_fma_f32 v[50:51], v[26:27], v[50:51], v[30:31]
	v_lshlrev_b32_e32 v56, 16, v54
	v_sub_f32_e32 v52, v52, v56
	v_and_b32_e32 v56, 0xffff0000, v54
	v_sub_f32_e32 v53, v53, v56
	v_cvt_pk_bf16_f32 v55, v50, v51
	v_cvt_pk_bf16_f32 v52, v52, v53
	s_nop 0
	v_lshlrev_b32_e32 v53, 16, v55
	v_sub_f32_e32 v50, v50, v53
	v_and_b32_e32 v53, 0xffff0000, v55
	v_sub_f32_e32 v51, v51, v53
	v_cvt_pk_bf16_f32 v53, v50, v51
	v_lshl_add_u32 v50, v32, 3, s76
	ds_write2st64_b64 v50, v[54:55], v[52:53] offset1:66
	v_lshlrev_b32_e32 v51, 16, v48
	v_and_b32_e32 v54, 0xffff0000, v48
	v_mov_b32_e32 v48, s69
	v_lshlrev_b32_e32 v52, 16, v49
	v_and_b32_e32 v53, 0xffff0000, v49
	ds_read_b64 v[48:49], v48
	s_waitcnt lgkmcnt(0)
	v_sub_f32_e32 v55, v54, v48
	v_sub_f32_e32 v54, v51, v48
	v_sub_f32_e32 v53, v53, v48
	v_sub_f32_e32 v52, v52, v48
	v_pk_mul_f32 v[54:55], v[48:49], v[54:55] op_sel:[1,0]
	v_pk_mul_f32 v[48:49], v[48:49], v[52:53] op_sel:[1,0]
	v_pk_fma_f32 v[52:53], v[24:25], v[54:55], v[28:29]
	v_pk_fma_f32 v[48:49], v[26:27], v[48:49], v[30:31]
	v_cvt_pk_bf16_f32 v54, v52, v53
	s_nop 0
	v_lshlrev_b32_e32 v51, 16, v54
	v_sub_f32_e32 v51, v52, v51
	v_and_b32_e32 v52, 0xffff0000, v54
	v_sub_f32_e32 v52, v53, v52
	v_cvt_pk_bf16_f32 v55, v48, v49
	v_cvt_pk_bf16_f32 v52, v51, v52
	s_nop 0
	v_lshlrev_b32_e32 v51, 16, v55
	v_sub_f32_e32 v48, v48, v51
	v_and_b32_e32 v51, 0xffff0000, v55
	v_sub_f32_e32 v49, v49, v51
	v_cvt_pk_bf16_f32 v53, v48, v49
	v_add_u32_e32 v48, 0x80, v50
	ds_write2st64_b64 v48, v[54:55], v[52:53] offset0:8 offset1:74
	v_lshlrev_b32_e32 v49, 16, v46
	v_and_b32_e32 v51, 0xffff0000, v46
	v_mov_b32_e32 v46, s41
	v_lshlrev_b32_e32 v52, 16, v47
	v_and_b32_e32 v53, 0xffff0000, v47
	ds_read_b64 v[46:47], v46
	s_waitcnt lgkmcnt(0)
	v_sub_f32_e32 v55, v51, v46
	v_sub_f32_e32 v54, v49, v46
	v_sub_f32_e32 v53, v53, v46
	v_sub_f32_e32 v52, v52, v46
	v_pk_mul_f32 v[54:55], v[46:47], v[54:55] op_sel:[1,0]
	v_pk_mul_f32 v[46:47], v[46:47], v[52:53] op_sel:[1,0]
	v_pk_fma_f32 v[52:53], v[24:25], v[54:55], v[28:29]
	v_pk_fma_f32 v[46:47], v[26:27], v[46:47], v[30:31]
	v_cvt_pk_bf16_f32 v54, v52, v53
	s_nop 0
	v_lshlrev_b32_e32 v49, 16, v54
	v_sub_f32_e32 v49, v52, v49
	v_and_b32_e32 v51, 0xffff0000, v54
	v_cvt_pk_bf16_f32 v55, v46, v47
	v_sub_f32_e32 v51, v53, v51
	v_cvt_pk_bf16_f32 v52, v49, v51
	v_lshlrev_b32_e32 v49, 16, v55
	v_sub_f32_e32 v46, v46, v49
	v_and_b32_e32 v49, 0xffff0000, v55
	v_sub_f32_e32 v47, v47, v49
	v_cvt_pk_bf16_f32 v53, v46, v47
	v_add_u32_e32 v46, 0x100, v50
	ds_write2st64_b64 v46, v[54:55], v[52:53] offset0:16 offset1:82
	v_lshlrev_b32_e32 v47, 16, v44
	v_and_b32_e32 v49, 0xffff0000, v44
	v_mov_b32_e32 v44, s47
	v_lshlrev_b32_e32 v51, 16, v45
	v_and_b32_e32 v52, 0xffff0000, v45
	ds_read_b64 v[44:45], v44
	s_waitcnt lgkmcnt(0)
	v_sub_f32_e32 v55, v49, v44
	v_sub_f32_e32 v54, v47, v44
	v_sub_f32_e32 v53, v52, v44
	v_sub_f32_e32 v52, v51, v44
	v_pk_mul_f32 v[54:55], v[44:45], v[54:55] op_sel:[1,0]
	v_pk_mul_f32 v[44:45], v[44:45], v[52:53] op_sel:[1,0]
	v_pk_fma_f32 v[52:53], v[24:25], v[54:55], v[28:29]
	v_pk_fma_f32 v[44:45], v[26:27], v[44:45], v[30:31]
	v_cvt_pk_bf16_f32 v54, v52, v53
	v_and_b32_e32 v51, 0xffff0000, v43
	v_lshlrev_b32_e32 v47, 16, v54
	v_sub_f32_e32 v47, v52, v47
	v_and_b32_e32 v49, 0xffff0000, v54
	v_cvt_pk_bf16_f32 v55, v44, v45
	v_sub_f32_e32 v49, v53, v49
	v_cvt_pk_bf16_f32 v52, v47, v49
	v_lshlrev_b32_e32 v47, 16, v55
	v_sub_f32_e32 v44, v44, v47
	v_and_b32_e32 v47, 0xffff0000, v55
	v_sub_f32_e32 v45, v45, v47
	v_cvt_pk_bf16_f32 v53, v44, v45
	v_add_u32_e32 v44, 0x180, v50
	ds_write2st64_b64 v44, v[54:55], v[52:53] offset0:24 offset1:90
	v_lshlrev_b32_e32 v45, 16, v42
	v_and_b32_e32 v47, 0xffff0000, v42
	v_mov_b32_e32 v42, s9
	v_lshlrev_b32_e32 v49, 16, v43
	ds_read_b64 v[42:43], v42
	s_waitcnt lgkmcnt(0)
	v_sub_f32_e32 v55, v47, v42
	v_sub_f32_e32 v54, v45, v42
	v_sub_f32_e32 v53, v51, v42
	v_sub_f32_e32 v52, v49, v42
	v_pk_mul_f32 v[54:55], v[42:43], v[54:55] op_sel:[1,0]
	v_pk_mul_f32 v[42:43], v[42:43], v[52:53] op_sel:[1,0]
	v_pk_fma_f32 v[52:53], v[24:25], v[54:55], v[28:29]
	v_pk_fma_f32 v[42:43], v[26:27], v[42:43], v[30:31]
	v_cvt_pk_bf16_f32 v54, v52, v53
	s_nop 0
	v_lshlrev_b32_e32 v45, 16, v54
	v_sub_f32_e32 v45, v52, v45
	v_and_b32_e32 v47, 0xffff0000, v54
	v_cvt_pk_bf16_f32 v55, v42, v43
	v_sub_f32_e32 v47, v53, v47
	v_cvt_pk_bf16_f32 v52, v45, v47
	v_lshlrev_b32_e32 v45, 16, v55
	v_sub_f32_e32 v42, v42, v45
	v_and_b32_e32 v45, 0xffff0000, v55
	v_sub_f32_e32 v43, v43, v45
	v_cvt_pk_bf16_f32 v53, v42, v43
	ds_write2st64_b64 v50, v[54:55], v[52:53] offset0:33 offset1:99
	v_lshlrev_b32_e32 v45, 16, v40
	v_and_b32_e32 v47, 0xffff0000, v40
	v_mov_b32_e32 v40, s0
	v_lshlrev_b32_e32 v42, 16, v41
	v_and_b32_e32 v43, 0xffff0000, v41
	ds_read_b64 v[40:41], v40
	s_waitcnt lgkmcnt(0)
; #define LAS __attribute__((address_space(3)))
; __device__ __forceinline__ unsigned cvt_pk_bf16(float lo, float hi) { unsigned r; asm volatile("v_cvt_pk_bf16_f32 %0, %1, %2" : "=v"(r) : "v"(lo), "v"(hi)); return r; }
; #define FLANE lane_id()
; __device__ __forceinline__ void p6_router(Frame& F) {
;     ...
;               for (int i = 0; i < 8; ++i) { const int r = F.wave + 8 * i; const v2u zw = zp[i];
;                 const f32x4 zv = (f32x4){bf_lo(zw.x), bf_hi(zw.x), bf_lo(zw.y), bf_hi(zw.y)};
;                 const f32x4 hh = (zv - stl[2 * r]) * stl[2 * r + 1] * g + b;
;                 v2u hi, lo; hi.x = cvt_pk_bf16(hh[0], hh[1]); hi.y = cvt_pk_bf16(hh[2], hh[3]);
;                 lo.x = cvt_pk_bf16(hh[0] - bf_lo(hi.x), hh[1] - bf_hi(hi.x)); lo.y = cvt_pk_bf16(hh[2] - bf_lo(hi.y), hh[3] - bf_hi(hi.y));
;                 *(LAS v2u*)(Hhi + r * HP + ln * 8) = hi; *(LAS v2u*)(Hlo + r * HP + ln * 8) = lo; }
; #pragma unroll
;               for (int i = 0; i < 4; ++i) { const int q = F.wave * 64 + ln + NTHR * i, e = (q >> 5) & 31, c8 = q & 31; *(LAS v4u*)(((q >> 10) ? Wlo : Whi) + e * HP + c8 * 16) = wp[i]; } }
;             __syncthreads();
;             if (kc + 1 < 8) P6_LOAD(kc + 1);
;             { const int ln = FLANE, fr = ln & 15, fq = ln >> 4;
; #pragma unroll
;               for (int ks = 0; ks < 4; ++ks) { const int kb = (kh * 128 + ks * 32 + fq * 8) * 2;
;                 const bf16x8 th = __builtin_bit_cast(bf16x8, *(const LAS i32x4*)(Hhi + (tt * 16 + fr) * HP + kb)), tl = __builtin_bit_cast(bf16x8, *(const LAS i32x4*)(Hlo + (tt * 16 + fr) * HP + kb));
; #pragma unroll
;                 for (int et = 0; et < 2; ++et) { const bf16x8 wh = __builtin_bit_cast(bf16x8, *(const LAS i32x4*)(Whi + (et * 16 + fr) * HP + kb)), wl = __builtin_bit_cast(bf16x8, *(const LAS i32x4*)(Wlo + (et * 16 + fr) * HP + kb));
;                     ac[et] = __builtin_amdgcn_mfma_f32_16x16x32_bf16(wh, th, ac[et], 0, 0, 0); ac[et] = __builtin_amdgcn_mfma_f32_16x16x32_bf16(wl, th, ac[et], 0, 0, 0); ac[et] = __builtin_amdgcn_mfma_f32_16x16x32_bf16(wh, tl, ac[et], 0, 0, 0); } } }
	v_sub_f32_e32 v51, v47, v40
	v_sub_f32_e32 v50, v45, v40
	v_sub_f32_e32 v43, v43, v40
	v_sub_f32_e32 v42, v42, v40
	v_pk_mul_f32 v[50:51], v[40:41], v[50:51] op_sel:[1,0]
	v_pk_mul_f32 v[40:41], v[40:41], v[42:43] op_sel:[1,0]
	v_pk_fma_f32 v[42:43], v[24:25], v[50:51], v[28:29]
	v_pk_fma_f32 v[40:41], v[26:27], v[40:41], v[30:31]
	v_cvt_pk_bf16_f32 v50, v42, v43
	s_nop 0
	v_lshlrev_b32_e32 v45, 16, v50
	v_sub_f32_e32 v42, v42, v45
	v_and_b32_e32 v45, 0xffff0000, v50
	v_sub_f32_e32 v43, v43, v45
	v_cvt_pk_bf16_f32 v51, v40, v41
	v_cvt_pk_bf16_f32 v42, v42, v43
	s_nop 0
	v_lshlrev_b32_e32 v43, 16, v51
	v_sub_f32_e32 v40, v40, v43
	v_and_b32_e32 v43, 0xffff0000, v51
	v_sub_f32_e32 v41, v41, v43
	v_cvt_pk_bf16_f32 v43, v40, v41
	ds_write2st64_b64 v48, v[50:51], v[42:43] offset0:41 offset1:107
	v_lshlrev_b32_e32 v42, 16, v38
	v_and_b32_e32 v43, 0xffff0000, v38
	v_mov_b32_e32 v38, s51
	v_lshlrev_b32_e32 v40, 16, v39
	v_and_b32_e32 v41, 0xffff0000, v39
	ds_read_b64 v[38:39], v38
	s_waitcnt lgkmcnt(0)
	v_sub_f32_e32 v43, v43, v38
	v_sub_f32_e32 v42, v42, v38
	v_sub_f32_e32 v41, v41, v38
	v_sub_f32_e32 v40, v40, v38
	v_pk_mul_f32 v[42:43], v[38:39], v[42:43] op_sel:[1,0]
	v_pk_mul_f32 v[38:39], v[38:39], v[40:41] op_sel:[1,0]
	v_pk_fma_f32 v[40:41], v[24:25], v[42:43], v[28:29]
	v_pk_fma_f32 v[38:39], v[26:27], v[38:39], v[30:31]
	v_cvt_pk_bf16_f32 v42, v40, v41
	s_nop 0
	v_lshlrev_b32_e32 v45, 16, v42
	v_sub_f32_e32 v40, v40, v45
	v_and_b32_e32 v45, 0xffff0000, v42
	v_sub_f32_e32 v41, v41, v45
	v_cvt_pk_bf16_f32 v43, v38, v39
	v_cvt_pk_bf16_f32 v40, v40, v41
	s_nop 0
	v_lshlrev_b32_e32 v41, 16, v43
	v_sub_f32_e32 v38, v38, v41
	v_and_b32_e32 v41, 0xffff0000, v43
	v_sub_f32_e32 v39, v39, v41
	v_cvt_pk_bf16_f32 v41, v38, v39
	ds_write2st64_b64 v46, v[42:43], v[40:41] offset0:49 offset1:115
	v_lshlrev_b32_e32 v40, 16, v36
	v_and_b32_e32 v41, 0xffff0000, v36
	v_mov_b32_e32 v36, s46
	v_lshlrev_b32_e32 v38, 16, v37
	v_and_b32_e32 v39, 0xffff0000, v37
	ds_read_b64 v[36:37], v36
	s_waitcnt lgkmcnt(0)
	v_sub_f32_e32 v39, v39, v36
	v_sub_f32_e32 v38, v38, v36
	v_sub_f32_e32 v41, v41, v36
	v_sub_f32_e32 v40, v40, v36
	v_pk_mul_f32 v[40:41], v[36:37], v[40:41] op_sel:[1,0]
	v_pk_mul_f32 v[36:37], v[36:37], v[38:39] op_sel:[1,0]
	v_pk_fma_f32 v[24:25], v[24:25], v[40:41], v[28:29]
	v_pk_fma_f32 v[26:27], v[26:27], v[36:37], v[30:31]
	v_cvt_pk_bf16_f32 v28, v24, v25
	s_nop 0
	v_lshlrev_b32_e32 v30, 16, v28
	v_sub_f32_e32 v24, v24, v30
	v_and_b32_e32 v30, 0xffff0000, v28
	v_sub_f32_e32 v25, v25, v30
	v_cvt_pk_bf16_f32 v29, v26, v27
	v_cvt_pk_bf16_f32 v24, v24, v25
	s_nop 0
	v_lshlrev_b32_e32 v25, 16, v29
	v_sub_f32_e32 v25, v26, v25
	v_and_b32_e32 v26, 0xffff0000, v29
	v_sub_f32_e32 v26, v27, v26
	v_cvt_pk_bf16_f32 v25, v25, v26
	ds_write2st64_b64 v44, v[28:29], v[24:25] offset0:57 offset1:123
	v_lshlrev_b32_e32 v24, 4, v32
	v_and_b32_e32 v26, 0x1f0, v24
	v_add_u32_e32 v24, s88, v32
	v_bfe_u32 v27, v24, 5, 5
	v_cmp_gt_u32_e32 vcc, s20, v24
	v_mov_b32_e32 v24, s66
	v_mov_b32_e32 v25, s80
	v_cndmask_b32_e32 v28, v24, v25, vcc
	v_mul_u32_u24_e32 v27, 0x210, v27
	v_add3_u32 v27, v28, v27, v26
	ds_write_b128 v27, v[8:11]
	v_add_u32_e32 v8, s86, v32
	v_bfe_u32 v9, v8, 5, 5
	v_cmp_gt_u32_e32 vcc, s20, v8
	v_mul_u32_u24_e32 v9, 0x210, v9
	s_nop 0
	v_cndmask_b32_e32 v8, v24, v25, vcc
	v_add3_u32 v8, v8, v9, v26
	ds_write_b128 v8, v[20:23]
	v_add_u32_e32 v8, s21, v32
	v_bfe_u32 v9, v8, 5, 5
	v_cmp_gt_u32_e32 vcc, s20, v8
	v_mul_u32_u24_e32 v9, 0x210, v9
	s_nop 0
	v_cndmask_b32_e32 v8, v24, v25, vcc
	v_add3_u32 v8, v8, v9, v26
	ds_write_b128 v8, v[16:19]
	v_add_u32_e32 v8, s87, v32
	v_bfe_u32 v9, v8, 5, 5
	v_cmp_gt_u32_e32 vcc, s20, v8
	v_mul_u32_u24_e32 v9, 0x210, v9
	s_nop 0
	v_cndmask_b32_e32 v8, v24, v25, vcc
	v_add3_u32 v8, v8, v9, v26
	ds_write_b128 v8, v[12:15]
	s_waitcnt lgkmcnt(0)
	s_barrier
	v_mbcnt_lo_u32_b32 v12, -1, 0
	v_mbcnt_hi_u32_b32 v12, -1, v12
	s_nop 0
	v_lshlrev_b32_e32 v8, 2, v12
	v_ashrrev_i32_e32 v9, 31, v8
	v_lshlrev_b64 v[8:9], 1, v[8:9]
	v_lshl_add_u64 v[10:11], s[6:7], 0, v[8:9]
	s_add_u32 s6, s28, s33
	s_addc_u32 s7, s29, s43
	global_load_dwordx2 v[50:51], v[10:11], off
	v_lshl_add_u64 v[10:11], s[6:7], 0, v[8:9]
	s_add_u32 s6, s28, s45
	s_addc_u32 s7, s29, s49
	global_load_dwordx2 v[48:49], v[10:11], off
	v_lshl_add_u64 v[10:11], s[6:7], 0, v[8:9]
	s_add_u32 s6, s28, s53
	s_addc_u32 s7, s29, s62
	global_load_dwordx2 v[46:47], v[10:11], off
	v_lshl_add_u64 v[10:11], s[6:7], 0, v[8:9]
	s_add_u32 s6, s28, s55
	s_addc_u32 s7, s29, s63
	global_load_dwordx2 v[44:45], v[10:11], off
	v_lshl_add_u64 v[10:11], s[6:7], 0, v[8:9]
	s_add_u32 s6, s28, s57
	s_addc_u32 s7, s29, s89
	global_load_dwordx2 v[42:43], v[10:11], off
	v_lshl_add_u64 v[10:11], s[6:7], 0, v[8:9]
	s_add_u32 s6, s28, s59
	s_addc_u32 s7, s29, s74
	global_load_dwordx2 v[40:41], v[10:11], off
	v_lshl_add_u64 v[10:11], s[6:7], 0, v[8:9]
	s_add_u32 s6, s28, s61
	v_add_u32_e32 v13, s88, v12
	s_addc_u32 s7, s29, s10
	v_add_u32_e32 v14, 0x200, v13
	v_lshl_add_u64 v[8:9], s[6:7], 0, v[8:9]
	v_ashrrev_i32_e32 v14, 5, v14
	global_load_dwordx2 v[38:39], v[10:11], off
	global_load_dwordx2 v[36:37], v[8:9], off
	v_lshlrev_b32_e32 v10, 4, v12
	v_ashrrev_i32_e32 v15, 31, v14
	v_and_b32_e32 v12, 0x1f0, v10
	s_add_u32 s6, s28, s4
	v_lshlrev_b64 v[14:15], 12, v[14:15]
	s_addc_u32 s7, s29, s5
	v_or_b32_e32 v14, v14, v12
	v_lshl_add_u64 v[14:15], s[6:7], 0, v[14:15]
	global_load_dwordx4 v[20:23], v[14:15], off
	v_add_u32_e32 v14, 0x400, v13
	v_ashrrev_i32_e32 v14, 5, v14
	v_ashrrev_i32_e32 v15, 31, v14
	v_lshlrev_b64 v[14:15], 12, v[14:15]
	v_or_b32_e32 v14, v14, v12
	v_ashrrev_i32_e32 v8, 5, v13
	v_lshl_add_u64 v[14:15], s[6:7], 0, v[14:15]
	v_add_u32_e32 v13, 0x600, v13
	global_load_dwordx4 v[16:19], v[14:15], off
	v_ashrrev_i32_e32 v14, 5, v13
	v_ashrrev_i32_e32 v9, 31, v8
	v_ashrrev_i32_e32 v15, 31, v14
	v_lshlrev_b64 v[8:9], 12, v[8:9]
	v_lshlrev_b64 v[14:15], 12, v[14:15]
	v_or_b32_e32 v8, v8, v12
	v_or_b32_e32 v14, v14, v12
	v_lshl_add_u64 v[8:9], s[6:7], 0, v[8:9]
	v_lshl_add_u64 v[12:13], s[6:7], 0, v[14:15]
	global_load_dwordx4 v[8:11], v[8:9], off
	s_addk_i32 s40, 0x100
	global_load_dwordx4 v[12:15], v[12:13], off
	v_mbcnt_lo_u32_b32 v26, -1, 0
	v_mbcnt_hi_u32_b32 v26, -1, v26
	s_add_u32 s2, s2, 0x200
	v_and_b32_e32 v30, 15, v26
	v_and_b32_e32 v26, -16, v26
	v_add_u32_e32 v32, s82, v26
	v_or_b32_e32 v26, s83, v30
	v_mul_u32_u24_e32 v26, 0x210, v26
	v_mad_u32_u24 v66, v30, s90, v25
	v_add3_u32 v65, 0, v26, v32
	v_add_u32_e32 v25, v66, v32
	ds_read_b128 v[26:29], v65
	ds_read_b128 v[52:55], v65 offset:33792
	ds_read_b128 v[56:59], v25
	v_mad_u32_u24 v67, v30, s90, v24
	v_add_u32_e32 v24, v67, v32
	ds_read_b128 v[60:63], v24
	s_waitcnt lgkmcnt(1)
; #define LAS __attribute__((address_space(3)))
; #define FLANE lane_id()
; __device__ __forceinline__ void p6_router(Frame& F) {
;     ...
;             { const int ln = FLANE, fr = ln & 15, fq = ln >> 4;
; #pragma unroll
;               for (int ks = 0; ks < 4; ++ks) { const int kb = (kh * 128 + ks * 32 + fq * 8) * 2;
;                 const bf16x8 th = __builtin_bit_cast(bf16x8, *(const LAS i32x4*)(Hhi + (tt * 16 + fr) * HP + kb)), tl = __builtin_bit_cast(bf16x8, *(const LAS i32x4*)(Hlo + (tt * 16 + fr) * HP + kb));
; #pragma unroll
;                 for (int et = 0; et < 2; ++et) { const bf16x8 wh = __builtin_bit_cast(bf16x8, *(const LAS i32x4*)(Whi + (et * 16 + fr) * HP + kb)), wl = __builtin_bit_cast(bf16x8, *(const LAS i32x4*)(Wlo + (et * 16 + fr) * HP + kb));
;                     ac[et] = __builtin_amdgcn_mfma_f32_16x16x32_bf16(wh, th, ac[et], 0, 0, 0); ac[et] = __builtin_amdgcn_mfma_f32_16x16x32_bf16(wl, th, ac[et], 0, 0, 0); ac[et] = __builtin_amdgcn_mfma_f32_16x16x32_bf16(wh, tl, ac[et], 0, 0, 0); } } }
;             __syncthreads();
;         }
	v_mfma_f32_16x16x32_bf16 v[4:7], v[56:59], v[26:29], v[4:7]
	v_mul_u32_u24_e32 v64, 0x210, v30
	s_addc_u32 s8, s8, 0
	s_add_u32 s33, s33, 0x200
	s_waitcnt lgkmcnt(0)
	v_mfma_f32_16x16x32_bf16 v[4:7], v[60:63], v[26:29], v[4:7]
	s_addc_u32 s43, s43, 0
	s_add_u32 s45, s45, 0x200
	s_addc_u32 s49, s49, 0
	v_mfma_f32_16x16x32_bf16 v[4:7], v[56:59], v[52:55], v[4:7]
	ds_read_b128 v[56:59], v25 offset:8448
	ds_read_b128 v[60:63], v24 offset:8448
	s_add_u32 s53, s53, 0x200
	s_addc_u32 s62, s62, 0
	s_waitcnt lgkmcnt(1)
	v_mfma_f32_16x16x32_bf16 v[0:3], v[56:59], v[26:29], v[0:3]
	s_add_u32 s55, s55, 0x200
	s_addc_u32 s63, s63, 0
	s_add_u32 s57, s57, 0x200
	s_waitcnt lgkmcnt(0)
	v_mfma_f32_16x16x32_bf16 v[0:3], v[60:63], v[26:29], v[0:3]
	v_add_u32_e32 v60, 64, v32
	ds_read_b128 v[24:27], v65 offset:64
	ds_read_b128 v[28:31], v65 offset:33856
	s_addc_u32 s89, s89, 0
	v_mfma_f32_16x16x32_bf16 v[0:3], v[56:59], v[52:55], v[0:3]
	v_add_u32_e32 v52, v66, v60
	ds_read_b128 v[52:55], v52
	v_add_u32_e32 v56, v67, v60
	ds_read_b128 v[56:59], v56
	s_waitcnt lgkmcnt(1)
	v_mfma_f32_16x16x32_bf16 v[4:7], v[52:55], v[24:27], v[4:7]
	s_add_u32 s59, s59, 0x200
	s_addc_u32 s74, s74, 0
	s_add_u32 s61, s61, 0x200
	s_waitcnt lgkmcnt(0)
	v_mfma_f32_16x16x32_bf16 v[4:7], v[56:59], v[24:27], v[4:7]
	v_add3_u32 v56, s66, v60, v64
	ds_read_b128 v[56:59], v56 offset:8448
	s_addc_u32 s10, s10, 0
	v_mfma_f32_16x16x32_bf16 v[4:7], v[52:55], v[28:31], v[4:7]
	v_add3_u32 v52, s80, v60, v64
	ds_read_b128 v[52:55], v52 offset:8448
	v_add_u32_e32 v60, 0x80, v32
	s_waitcnt lgkmcnt(0)
	v_mfma_f32_16x16x32_bf16 v[0:3], v[52:55], v[24:27], v[0:3]
	v_add_u32_e32 v32, 0xc0, v32
	s_add_u32 s4, s4, 0x200
	s_addc_u32 s5, s5, 0
	v_mfma_f32_16x16x32_bf16 v[0:3], v[56:59], v[24:27], v[0:3]
	v_add_u32_e32 v56, v67, v60
	s_cmpk_eq_i32 s40, 0x700
	v_mfma_f32_16x16x32_bf16 v[0:3], v[52:55], v[28:31], v[0:3]
	v_add_u32_e32 v52, v66, v60
	ds_read_b128 v[24:27], v65 offset:128
	ds_read_b128 v[28:31], v65 offset:33920
	ds_read_b128 v[52:55], v52
	ds_read_b128 v[56:59], v56
	s_waitcnt lgkmcnt(1)
	v_mfma_f32_16x16x32_bf16 v[4:7], v[52:55], v[24:27], v[4:7]
	s_waitcnt lgkmcnt(0)
	v_mfma_f32_16x16x32_bf16 v[4:7], v[56:59], v[24:27], v[4:7]
	v_add3_u32 v56, s66, v60, v64
	ds_read_b128 v[56:59], v56 offset:8448
	v_mfma_f32_16x16x32_bf16 v[4:7], v[52:55], v[28:31], v[4:7]
	v_add3_u32 v52, s80, v60, v64
	ds_read_b128 v[52:55], v52 offset:8448
	s_waitcnt lgkmcnt(0)
	v_mfma_f32_16x16x32_bf16 v[0:3], v[52:55], v[24:27], v[0:3]
	v_mfma_f32_16x16x32_bf16 v[0:3], v[56:59], v[24:27], v[0:3]
	v_add_u32_e32 v56, v67, v32
	v_mfma_f32_16x16x32_bf16 v[0:3], v[52:55], v[28:31], v[0:3]
	v_add_u32_e32 v52, v66, v32
	ds_read_b128 v[24:27], v65 offset:192
	ds_read_b128 v[28:31], v65 offset:33984
	ds_read_b128 v[52:55], v52
	ds_read_b128 v[56:59], v56
	s_waitcnt lgkmcnt(1)
	v_mfma_f32_16x16x32_bf16 v[4:7], v[52:55], v[24:27], v[4:7]
	s_waitcnt lgkmcnt(0)
	v_mfma_f32_16x16x32_bf16 v[4:7], v[56:59], v[24:27], v[4:7]
	v_mfma_f32_16x16x32_bf16 v[4:7], v[52:55], v[28:31], v[4:7]
	v_add3_u32 v52, s80, v32, v64
	ds_read_b128 v[52:55], v52 offset:8448
	v_add3_u32 v32, s66, v32, v64
	ds_read_b128 v[56:59], v32 offset:8448
	s_waitcnt lgkmcnt(1)
	v_mfma_f32_16x16x32_bf16 v[0:3], v[52:55], v[24:27], v[0:3]
	s_waitcnt lgkmcnt(0)
	s_barrier
	v_mfma_f32_16x16x32_bf16 v[0:3], v[56:59], v[24:27], v[0:3]
	v_mfma_f32_16x16x32_bf16 v[0:3], v[52:55], v[28:31], v[0:3]
	s_cbranch_scc0 .LBB0_1500
	v_mbcnt_lo_u32_b32 v32, -1, 0
	v_mbcnt_hi_u32_b32 v32, -1, v32
	s_waitcnt vmcnt(11)
	v_lshlrev_b32_e32 v54, 16, v50
	v_lshlrev_b32_e32 v24, 2, v32
	v_ashrrev_i32_e32 v25, 31, v24
	v_lshl_add_u64 v[28:29], v[24:25], 2, v[34:35]
	v_lshl_add_u64 v[24:25], s[12:13], 0, v[28:29]
	v_lshl_add_u64 v[28:29], s[14:15], 0, v[28:29]
	global_load_dwordx4 v[24:27], v[24:25], off
	v_and_b32_e32 v55, 0xffff0000, v50
	global_load_dwordx4 v[28:31], v[28:29], off
	v_mov_b32_e32 v50, s67
	v_lshlrev_b32_e32 v52, 16, v51
	v_and_b32_e32 v53, 0xffff0000, v51
	ds_read_b64 v[50:51], v50
	v_readlane_b32 s4, v255, 22
	v_readlane_b32 s5, v255, 23
	s_waitcnt lgkmcnt(0)
	v_sub_f32_e32 v55, v55, v50
	v_sub_f32_e32 v54, v54, v50
	v_sub_f32_e32 v53, v53, v50
	v_sub_f32_e32 v52, v52, v50
	v_pk_mul_f32 v[54:55], v[50:51], v[54:55] op_sel:[1,0]
	v_pk_mul_f32 v[50:51], v[50:51], v[52:53] op_sel:[1,0]
	s_waitcnt vmcnt(0)
	v_pk_fma_f32 v[52:53], v[24:25], v[54:55], v[28:29]
	s_nop 0
	v_cvt_pk_bf16_f32 v54, v52, v53
	v_pk_fma_f32 v[50:51], v[26:27], v[50:51], v[30:31]
	v_lshlrev_b32_e32 v56, 16, v54
	v_sub_f32_e32 v52, v52, v56
	v_and_b32_e32 v56, 0xffff0000, v54
	v_sub_f32_e32 v53, v53, v56
	v_cvt_pk_bf16_f32 v55, v50, v51
	v_cvt_pk_bf16_f32 v52, v52, v53
	s_nop 0
	v_lshlrev_b32_e32 v53, 16, v55
	v_sub_f32_e32 v50, v50, v53
	v_and_b32_e32 v53, 0xffff0000, v55
	v_sub_f32_e32 v51, v51, v53
	v_cvt_pk_bf16_f32 v53, v50, v51
	v_lshl_add_u32 v50, v32, 3, s76
	ds_write2st64_b64 v50, v[54:55], v[52:53] offset1:66
	v_lshlrev_b32_e32 v51, 16, v48
	v_and_b32_e32 v54, 0xffff0000, v48
	v_mov_b32_e32 v48, s69
	v_lshlrev_b32_e32 v52, 16, v49
	v_and_b32_e32 v53, 0xffff0000, v49
	ds_read_b64 v[48:49], v48
	s_waitcnt lgkmcnt(0)
; #define GAS __attribute__((address_space(1)))
; #define LAS __attribute__((address_space(3)))
; __device__ __forceinline__ unsigned cvt_pk_bf16(float lo, float hi) { unsigned r; asm volatile("v_cvt_pk_bf16_f32 %0, %1, %2" : "=v"(r) : "v"(lo), "v"(hi)); return r; }
; #define FLANE lane_id()
; __device__ __forceinline__ void p6_router(Frame& F) {
;     ...
;             { const int ln = FLANE, col = kc * 256 + ln * 4; const f32x4 g = *(const GAS f32x4*)(F.ln1_g + col), b = *(const GAS f32x4*)(F.ln1_b + col);
; #pragma unroll
;               for (int i = 0; i < 8; ++i) { const int r = F.wave + 8 * i; const v2u zw = zp[i];
;                 const f32x4 zv = (f32x4){bf_lo(zw.x), bf_hi(zw.x), bf_lo(zw.y), bf_hi(zw.y)};
;                 const f32x4 hh = (zv - stl[2 * r]) * stl[2 * r + 1] * g + b;
;                 v2u hi, lo; hi.x = cvt_pk_bf16(hh[0], hh[1]); hi.y = cvt_pk_bf16(hh[2], hh[3]);
;                 lo.x = cvt_pk_bf16(hh[0] - bf_lo(hi.x), hh[1] - bf_hi(hi.x)); lo.y = cvt_pk_bf16(hh[2] - bf_lo(hi.y), hh[3] - bf_hi(hi.y));
;                 *(LAS v2u*)(Hhi + r * HP + ln * 8) = hi; *(LAS v2u*)(Hlo + r * HP + ln * 8) = lo; }
	v_sub_f32_e32 v55, v54, v48
	v_sub_f32_e32 v54, v51, v48
	v_sub_f32_e32 v53, v53, v48
	v_sub_f32_e32 v52, v52, v48
	v_pk_mul_f32 v[54:55], v[48:49], v[54:55] op_sel:[1,0]
	v_pk_mul_f32 v[48:49], v[48:49], v[52:53] op_sel:[1,0]
	v_pk_fma_f32 v[52:53], v[24:25], v[54:55], v[28:29]
	v_pk_fma_f32 v[48:49], v[26:27], v[48:49], v[30:31]
	v_cvt_pk_bf16_f32 v54, v52, v53
	s_nop 0
	v_lshlrev_b32_e32 v51, 16, v54
	v_sub_f32_e32 v51, v52, v51
	v_and_b32_e32 v52, 0xffff0000, v54
	v_sub_f32_e32 v52, v53, v52
	v_cvt_pk_bf16_f32 v55, v48, v49
	v_cvt_pk_bf16_f32 v52, v51, v52
	s_nop 0
	v_lshlrev_b32_e32 v51, 16, v55
	v_sub_f32_e32 v48, v48, v51
	v_and_b32_e32 v51, 0xffff0000, v55
	v_sub_f32_e32 v49, v49, v51
	v_cvt_pk_bf16_f32 v53, v48, v49
	v_add_u32_e32 v48, 0x80, v50
	ds_write2st64_b64 v48, v[54:55], v[52:53] offset0:8 offset1:74
	v_lshlrev_b32_e32 v49, 16, v46
	v_and_b32_e32 v51, 0xffff0000, v46
	v_mov_b32_e32 v46, s41
	v_lshlrev_b32_e32 v52, 16, v47
	v_and_b32_e32 v53, 0xffff0000, v47
	ds_read_b64 v[46:47], v46
	s_waitcnt lgkmcnt(0)
	v_sub_f32_e32 v55, v51, v46
	v_sub_f32_e32 v54, v49, v46
	v_sub_f32_e32 v53, v53, v46
	v_sub_f32_e32 v52, v52, v46
	v_pk_mul_f32 v[54:55], v[46:47], v[54:55] op_sel:[1,0]
	v_pk_mul_f32 v[46:47], v[46:47], v[52:53] op_sel:[1,0]
	v_pk_fma_f32 v[52:53], v[24:25], v[54:55], v[28:29]
	v_pk_fma_f32 v[46:47], v[26:27], v[46:47], v[30:31]
	v_cvt_pk_bf16_f32 v54, v52, v53
	s_nop 0
	v_lshlrev_b32_e32 v49, 16, v54
	v_sub_f32_e32 v49, v52, v49
	v_and_b32_e32 v51, 0xffff0000, v54
	v_cvt_pk_bf16_f32 v55, v46, v47
	v_sub_f32_e32 v51, v53, v51
	v_cvt_pk_bf16_f32 v52, v49, v51
	v_lshlrev_b32_e32 v49, 16, v55
	v_sub_f32_e32 v46, v46, v49
	v_and_b32_e32 v49, 0xffff0000, v55
	v_sub_f32_e32 v47, v47, v49
	v_cvt_pk_bf16_f32 v53, v46, v47
	v_add_u32_e32 v46, 0x100, v50
	ds_write2st64_b64 v46, v[54:55], v[52:53] offset0:16 offset1:82
	v_lshlrev_b32_e32 v47, 16, v44
	v_and_b32_e32 v49, 0xffff0000, v44
	v_mov_b32_e32 v44, s47
	v_lshlrev_b32_e32 v51, 16, v45
	v_and_b32_e32 v52, 0xffff0000, v45
	ds_read_b64 v[44:45], v44
	s_waitcnt lgkmcnt(0)
	v_sub_f32_e32 v55, v49, v44
	v_sub_f32_e32 v54, v47, v44
	v_sub_f32_e32 v53, v52, v44
	v_sub_f32_e32 v52, v51, v44
	v_pk_mul_f32 v[54:55], v[44:45], v[54:55] op_sel:[1,0]
	v_pk_mul_f32 v[44:45], v[44:45], v[52:53] op_sel:[1,0]
	v_pk_fma_f32 v[52:53], v[24:25], v[54:55], v[28:29]
	v_pk_fma_f32 v[44:45], v[26:27], v[44:45], v[30:31]
	v_cvt_pk_bf16_f32 v54, v52, v53
	v_and_b32_e32 v51, 0xffff0000, v42
	v_lshlrev_b32_e32 v47, 16, v54
	v_sub_f32_e32 v47, v52, v47
	v_and_b32_e32 v49, 0xffff0000, v54
	v_cvt_pk_bf16_f32 v55, v44, v45
	v_sub_f32_e32 v49, v53, v49
	v_cvt_pk_bf16_f32 v52, v47, v49
	v_lshlrev_b32_e32 v47, 16, v55
	v_sub_f32_e32 v44, v44, v47
	v_and_b32_e32 v47, 0xffff0000, v55
	v_sub_f32_e32 v45, v45, v47
	v_add_u32_e32 v47, 0x180, v50
	v_cvt_pk_bf16_f32 v53, v44, v45
	ds_write2st64_b64 v47, v[54:55], v[52:53] offset0:24 offset1:90
	v_lshlrev_b32_e32 v49, 16, v42
	v_mov_b32_e32 v42, s9
	v_lshlrev_b32_e32 v44, 16, v43
	v_and_b32_e32 v45, 0xffff0000, v43
	ds_read_b64 v[42:43], v42
	s_waitcnt lgkmcnt(0)
	v_sub_f32_e32 v53, v51, v42
	v_sub_f32_e32 v52, v49, v42
	v_sub_f32_e32 v45, v45, v42
	v_sub_f32_e32 v44, v44, v42
	v_pk_mul_f32 v[52:53], v[42:43], v[52:53] op_sel:[1,0]
	v_pk_mul_f32 v[42:43], v[42:43], v[44:45] op_sel:[1,0]
	v_pk_fma_f32 v[44:45], v[24:25], v[52:53], v[28:29]
	v_pk_fma_f32 v[42:43], v[26:27], v[42:43], v[30:31]
	v_cvt_pk_bf16_f32 v52, v44, v45
	s_nop 0
	v_lshlrev_b32_e32 v49, 16, v52
	v_sub_f32_e32 v44, v44, v49
	v_and_b32_e32 v49, 0xffff0000, v52
	v_sub_f32_e32 v45, v45, v49
	v_cvt_pk_bf16_f32 v53, v42, v43
	v_cvt_pk_bf16_f32 v44, v44, v45
	s_nop 0
	v_lshlrev_b32_e32 v45, 16, v53
	v_sub_f32_e32 v42, v42, v45
	v_and_b32_e32 v45, 0xffff0000, v53
	v_sub_f32_e32 v43, v43, v45
	v_cvt_pk_bf16_f32 v45, v42, v43
	ds_write2st64_b64 v50, v[52:53], v[44:45] offset0:33 offset1:99
	v_lshlrev_b32_e32 v44, 16, v40
	v_and_b32_e32 v45, 0xffff0000, v40
	v_mov_b32_e32 v40, s0
	v_lshlrev_b32_e32 v42, 16, v41
	v_and_b32_e32 v43, 0xffff0000, v41
	ds_read_b64 v[40:41], v40
	v_readlane_b32 s0, v255, 19
	s_waitcnt lgkmcnt(0)
	v_sub_f32_e32 v45, v45, v40
	v_sub_f32_e32 v44, v44, v40
	v_sub_f32_e32 v43, v43, v40
	v_sub_f32_e32 v42, v42, v40
	v_pk_mul_f32 v[44:45], v[40:41], v[44:45] op_sel:[1,0]
	v_pk_mul_f32 v[40:41], v[40:41], v[42:43] op_sel:[1,0]
	v_pk_fma_f32 v[42:43], v[24:25], v[44:45], v[28:29]
	v_pk_fma_f32 v[40:41], v[26:27], v[40:41], v[30:31]
	v_cvt_pk_bf16_f32 v44, v42, v43
	s_nop 0
	v_lshlrev_b32_e32 v49, 16, v44
	v_sub_f32_e32 v42, v42, v49
	v_and_b32_e32 v49, 0xffff0000, v44
	v_sub_f32_e32 v43, v43, v49
	v_cvt_pk_bf16_f32 v45, v40, v41
	v_cvt_pk_bf16_f32 v42, v42, v43
	s_nop 0
	v_lshlrev_b32_e32 v43, 16, v45
	v_sub_f32_e32 v40, v40, v43
	v_and_b32_e32 v43, 0xffff0000, v45
	v_sub_f32_e32 v41, v41, v43
	v_cvt_pk_bf16_f32 v43, v40, v41
	ds_write2st64_b64 v48, v[44:45], v[42:43] offset0:41 offset1:107
	v_lshlrev_b32_e32 v42, 16, v38
	v_and_b32_e32 v43, 0xffff0000, v38
	v_mov_b32_e32 v38, s51
	v_lshlrev_b32_e32 v40, 16, v39
	v_and_b32_e32 v41, 0xffff0000, v39
	ds_read_b64 v[38:39], v38
	s_waitcnt lgkmcnt(0)
; #define LAS __attribute__((address_space(3)))
; #define FLANE lane_id()
; #define P6_LOAD(kc_) do { const int ln_ = FLANE; _Pragma("unroll") for (int i_ = 0; i_ < 8; ++i_) zp[i_] = *(const GAS v2u*)(z1 + (size_t)(t0 + F.wave + 8 * i_) * D + (kc_) * 256 + ln_ * 4); \
;         _Pragma("unroll") for (int i_ = 0; i_ < 4; ++i_) { const int q_ = F.wave * 64 + ln_ + NTHR * i_; wp[i_] = *(const GAS v4u*)(wrt + (size_t)(q_ >> 5) * D + (kc_) * 256 + (q_ & 31) * 8); } } while (0)
; __device__ __forceinline__ void p6_router(Frame& F) {
;     ...
;                 *(LAS v2u*)(Hhi + r * HP + ln * 8) = hi; *(LAS v2u*)(Hlo + r * HP + ln * 8) = lo; }
; #pragma unroll
;               for (int i = 0; i < 4; ++i) { const int q = F.wave * 64 + ln + NTHR * i, e = (q >> 5) & 31, c8 = q & 31; *(LAS v4u*)(((q >> 10) ? Wlo : Whi) + e * HP + c8 * 16) = wp[i]; } }
;             __syncthreads();
;             if (kc + 1 < 8) P6_LOAD(kc + 1);
;             { const int ln = FLANE, fr = ln & 15, fq = ln >> 4;
; #pragma unroll
;               for (int ks = 0; ks < 4; ++ks) { const int kb = (kh * 128 + ks * 32 + fq * 8) * 2;
;                 const bf16x8 th = __builtin_bit_cast(bf16x8, *(const LAS i32x4*)(Hhi + (tt * 16 + fr) * HP + kb)), tl = __builtin_bit_cast(bf16x8, *(const LAS i32x4*)(Hlo + (tt * 16 + fr) * HP + kb));
; #pragma unroll
;                 for (int et = 0; et < 2; ++et) { const bf16x8 wh = __builtin_bit_cast(bf16x8, *(const LAS i32x4*)(Whi + (et * 16 + fr) * HP + kb)), wl = __builtin_bit_cast(bf16x8, *(const LAS i32x4*)(Wlo + (et * 16 + fr) * HP + kb));
;                     ac[et] = __builtin_amdgcn_mfma_f32_16x16x32_bf16(wh, th, ac[et], 0, 0, 0); ac[et] = __builtin_amdgcn_mfma_f32_16x16x32_bf16(wl, th, ac[et], 0, 0, 0); ac[et] = __builtin_amdgcn_mfma_f32_16x16x32_bf16(wh, tl, ac[et], 0, 0, 0); } } }
;             __syncthreads();
	v_sub_f32_e32 v43, v43, v38
	v_sub_f32_e32 v42, v42, v38
	v_sub_f32_e32 v41, v41, v38
	v_sub_f32_e32 v40, v40, v38
	v_pk_mul_f32 v[42:43], v[38:39], v[42:43] op_sel:[1,0]
	v_pk_mul_f32 v[38:39], v[38:39], v[40:41] op_sel:[1,0]
	v_pk_fma_f32 v[40:41], v[24:25], v[42:43], v[28:29]
	v_pk_fma_f32 v[38:39], v[26:27], v[38:39], v[30:31]
	v_cvt_pk_bf16_f32 v42, v40, v41
	s_nop 0
	v_lshlrev_b32_e32 v44, 16, v42
	v_sub_f32_e32 v40, v40, v44
	v_and_b32_e32 v44, 0xffff0000, v42
	v_sub_f32_e32 v41, v41, v44
	v_cvt_pk_bf16_f32 v43, v38, v39
	v_cvt_pk_bf16_f32 v40, v40, v41
	s_nop 0
	v_lshlrev_b32_e32 v41, 16, v43
	v_sub_f32_e32 v38, v38, v41
	v_and_b32_e32 v41, 0xffff0000, v43
	v_sub_f32_e32 v39, v39, v41
	v_cvt_pk_bf16_f32 v41, v38, v39
	ds_write2st64_b64 v46, v[42:43], v[40:41] offset0:49 offset1:115
	v_lshlrev_b32_e32 v40, 16, v36
	v_and_b32_e32 v41, 0xffff0000, v36
	v_mov_b32_e32 v36, s46
	v_lshlrev_b32_e32 v38, 16, v37
	v_and_b32_e32 v39, 0xffff0000, v37
	ds_read_b64 v[36:37], v36
	s_waitcnt lgkmcnt(0)
	v_sub_f32_e32 v39, v39, v36
	v_sub_f32_e32 v38, v38, v36
	v_sub_f32_e32 v41, v41, v36
	v_sub_f32_e32 v40, v40, v36
	v_pk_mul_f32 v[40:41], v[36:37], v[40:41] op_sel:[1,0]
	v_pk_mul_f32 v[36:37], v[36:37], v[38:39] op_sel:[1,0]
	v_pk_fma_f32 v[24:25], v[24:25], v[40:41], v[28:29]
	v_pk_fma_f32 v[26:27], v[26:27], v[36:37], v[30:31]
	v_cvt_pk_bf16_f32 v28, v24, v25
	s_nop 0
	v_lshlrev_b32_e32 v30, 16, v28
	v_sub_f32_e32 v24, v24, v30
	v_and_b32_e32 v30, 0xffff0000, v28
	v_sub_f32_e32 v25, v25, v30
	v_cvt_pk_bf16_f32 v29, v26, v27
	v_cvt_pk_bf16_f32 v24, v24, v25
	s_nop 0
	v_lshlrev_b32_e32 v25, 16, v29
	v_sub_f32_e32 v25, v26, v25
	v_and_b32_e32 v26, 0xffff0000, v29
	v_sub_f32_e32 v26, v27, v26
	v_cvt_pk_bf16_f32 v25, v25, v26
	ds_write2st64_b64 v47, v[28:29], v[24:25] offset0:57 offset1:123
	v_add_u32_e32 v25, s88, v32
	v_lshlrev_b32_e32 v24, 4, v32
	v_bfe_u32 v26, v25, 5, 5
	v_cmp_gt_u32_e32 vcc, s20, v25
	v_mov_b32_e32 v25, s66
	v_mov_b32_e32 v27, s80
	v_and_b32_e32 v24, 0x1f0, v24
	v_cndmask_b32_e32 v28, v25, v27, vcc
	v_mul_u32_u24_e32 v26, 0x210, v26
	v_add3_u32 v26, v28, v26, v24
	ds_write_b128 v26, v[8:11]
	v_add_u32_e32 v8, s86, v32
	v_bfe_u32 v9, v8, 5, 5
	v_cmp_gt_u32_e32 vcc, s20, v8
	v_mul_u32_u24_e32 v9, 0x210, v9
	s_nop 0
	v_cndmask_b32_e32 v8, v25, v27, vcc
	v_add3_u32 v8, v8, v9, v24
	ds_write_b128 v8, v[20:23]
	v_add_u32_e32 v8, s21, v32
	v_bfe_u32 v9, v8, 5, 5
	v_cmp_gt_u32_e32 vcc, s20, v8
	v_mul_u32_u24_e32 v9, 0x210, v9
	s_nop 0
	v_cndmask_b32_e32 v8, v25, v27, vcc
	v_add3_u32 v8, v8, v9, v24
	ds_write_b128 v8, v[16:19]
	v_add_u32_e32 v8, s87, v32
	v_bfe_u32 v9, v8, 5, 5
	v_cmp_gt_u32_e32 vcc, s20, v8
	v_mul_u32_u24_e32 v9, 0x210, v9
	v_mov_b32_e32 v32, 0
	v_cndmask_b32_e32 v8, v25, v27, vcc
	v_add3_u32 v8, v8, v9, v24
	ds_write_b128 v8, v[12:15]
	s_waitcnt lgkmcnt(0)
	s_barrier
	v_mbcnt_lo_u32_b32 v8, -1, 0
	v_mbcnt_hi_u32_b32 v8, -1, v8
	s_nop 0
	v_and_b32_e32 v20, 15, v8
	v_and_b32_e32 v8, -16, v8
	v_add_u32_e32 v24, s82, v8
	v_or_b32_e32 v8, s83, v20
	v_mul_u32_u24_e32 v8, 0x210, v8
	v_mad_u32_u24 v27, v20, s90, v27
	v_add3_u32 v28, 0, v8, v24
	v_add_u32_e32 v29, v27, v24
	ds_read_b128 v[8:11], v28
	ds_read_b128 v[12:15], v28 offset:33792
	ds_read_b128 v[16:19], v29
	v_mad_u32_u24 v25, v20, s90, v25
	v_add_u32_e32 v30, v25, v24
	v_mul_u32_u24_e32 v26, 0x210, v20
	ds_read_b128 v[20:23], v30
	s_waitcnt lgkmcnt(1)
	v_mfma_f32_16x16x32_bf16 v[4:7], v[16:19], v[8:11], v[4:7]
	s_waitcnt lgkmcnt(0)
	v_mfma_f32_16x16x32_bf16 v[4:7], v[20:23], v[8:11], v[4:7]
	v_mfma_f32_16x16x32_bf16 v[4:7], v[16:19], v[12:15], v[4:7]
	ds_read_b128 v[16:19], v29 offset:8448
	ds_read_b128 v[20:23], v30 offset:8448
	v_add_u32_e32 v29, 64, v24
	s_waitcnt lgkmcnt(1)
	v_mfma_f32_16x16x32_bf16 v[0:3], v[16:19], v[8:11], v[0:3]
	s_waitcnt lgkmcnt(0)
	v_mfma_f32_16x16x32_bf16 v[0:3], v[20:23], v[8:11], v[0:3]
	v_add_u32_e32 v20, v25, v29
	v_mfma_f32_16x16x32_bf16 v[0:3], v[16:19], v[12:15], v[0:3]
	v_add_u32_e32 v16, v27, v29
	ds_read_b128 v[8:11], v28 offset:64
	ds_read_b128 v[12:15], v28 offset:33856
	ds_read_b128 v[16:19], v16
	ds_read_b128 v[20:23], v20
	s_waitcnt lgkmcnt(1)
	v_mfma_f32_16x16x32_bf16 v[4:7], v[16:19], v[8:11], v[4:7]
	s_waitcnt lgkmcnt(0)
	v_mfma_f32_16x16x32_bf16 v[4:7], v[20:23], v[8:11], v[4:7]
	v_add3_u32 v20, s66, v29, v26
	ds_read_b128 v[20:23], v20 offset:8448
	v_mfma_f32_16x16x32_bf16 v[4:7], v[16:19], v[12:15], v[4:7]
	v_add3_u32 v16, s80, v29, v26
	ds_read_b128 v[16:19], v16 offset:8448
	v_add_u32_e32 v29, 0x80, v24
	s_waitcnt lgkmcnt(0)
	v_mfma_f32_16x16x32_bf16 v[0:3], v[16:19], v[8:11], v[0:3]
	v_add_u32_e32 v24, 0xc0, v24
	v_mfma_f32_16x16x32_bf16 v[0:3], v[20:23], v[8:11], v[0:3]
	v_add_u32_e32 v20, v25, v29
	v_mfma_f32_16x16x32_bf16 v[0:3], v[16:19], v[12:15], v[0:3]
	v_add_u32_e32 v16, v27, v29
	ds_read_b128 v[8:11], v28 offset:128
	ds_read_b128 v[12:15], v28 offset:33920
	ds_read_b128 v[16:19], v16
	ds_read_b128 v[20:23], v20
	s_waitcnt lgkmcnt(1)
	v_mfma_f32_16x16x32_bf16 v[4:7], v[16:19], v[8:11], v[4:7]
	s_waitcnt lgkmcnt(0)
	v_mfma_f32_16x16x32_bf16 v[4:7], v[20:23], v[8:11], v[4:7]
	v_add3_u32 v20, s66, v29, v26
	ds_read_b128 v[20:23], v20 offset:8448
	v_mfma_f32_16x16x32_bf16 v[4:7], v[16:19], v[12:15], v[4:7]
	v_add3_u32 v16, s80, v29, v26
	ds_read_b128 v[16:19], v16 offset:8448
	s_waitcnt lgkmcnt(0)
	v_mfma_f32_16x16x32_bf16 v[0:3], v[16:19], v[8:11], v[0:3]
	v_mfma_f32_16x16x32_bf16 v[0:3], v[20:23], v[8:11], v[0:3]
	v_add_u32_e32 v20, v25, v24
	v_mfma_f32_16x16x32_bf16 v[0:3], v[16:19], v[12:15], v[0:3]
	v_add_u32_e32 v16, v27, v24
	ds_read_b128 v[8:11], v28 offset:192
	ds_read_b128 v[12:15], v28 offset:33984
	ds_read_b128 v[16:19], v16
	ds_read_b128 v[20:23], v20
	s_waitcnt lgkmcnt(1)
	v_mfma_f32_16x16x32_bf16 v[4:7], v[16:19], v[8:11], v[4:7]
	s_waitcnt lgkmcnt(0)
	v_mfma_f32_16x16x32_bf16 v[4:7], v[20:23], v[8:11], v[4:7]
	v_add3_u32 v20, s66, v24, v26
	ds_read_b128 v[20:23], v20 offset:8448
	v_mfma_f32_16x16x32_bf16 v[4:7], v[16:19], v[12:15], v[4:7]
	v_add3_u32 v16, s80, v24, v26
	ds_read_b128 v[16:19], v16 offset:8448
	s_waitcnt lgkmcnt(0)
	v_mfma_f32_16x16x32_bf16 v[0:3], v[16:19], v[8:11], v[0:3]
	s_barrier
; #define GAS __attribute__((address_space(1)))
; #define LAS __attribute__((address_space(3)))
; #define FLANE lane_id()
; __device__ __forceinline__ void p6_router(Frame& F) {
;     ...
;         { const int ln = FLANE, fr = ln & 15, fq = ln >> 4;
; #pragma unroll
;           for (int et = 0; et < 2; ++et) *(LAS f32x4*)(part + (kh * 64 + tt * 16 + fr) * 32 + et * 16 + 4 * fq) = ac[et];
;           __syncthreads();
;           { const int r = FTID >> 3, e0 = (FTID & 7) * 4;
;               const f32x4 a = *(const LAS f32x4*)(part + (0 * 64 + r) * 32 + e0), b = *(const LAS f32x4*)(part + (1 * 64 + r) * 32 + e0);
;               const f32x4 br = *(const GAS f32x4*)(F.b_r + e0), sum = (a + b) + br; LAS float* d = lg + r * 33 + e0; d[0] = sum[0]; d[1] = sum[1]; d[2] = sum[2]; d[3] = sum[3]; } }
;         __syncthreads();
;         int ek[4] = {0, 0, 0, 0}, lp[4] = {0, 0, 0, 0}; float gk[4] = {0.f, 0.f, 0.f, 0.f};
;         if (FTID < 64) {
;             float lv[4]; unsigned used = 0u;
; #pragma unroll
;             for (int k = 0; k < 4; ++k) { float best = -3.0e38f; int bi = 0;
;                 for (int e = 0; e < NE; ++e) { const float v = lg[FTID * 33 + e]; const bool ok = !((used >> e) & 1u) && (v > best); best = ok ? v : best; bi = ok ? e : bi; }
;                 used |= 1u << bi; ek[k] = bi; lv[k] = best; }
	v_mfma_f32_16x16x32_bf16 v[0:3], v[20:23], v[8:11], v[0:3]
	v_mbcnt_lo_u32_b32 v8, -1, 0
	v_mbcnt_hi_u32_b32 v8, -1, v8
	s_nop 0
	v_and_or_b32 v9, v8, 15, s0
	v_mfma_f32_16x16x32_bf16 v[0:3], v[16:19], v[12:15], v[0:3]
	v_lshlrev_b32_e32 v9, 7, v9
	v_and_b32_e32 v8, -16, v8
	v_add3_u32 v8, s68, v9, v8
	ds_write_b128 v8, v[4:7]
	s_nop 3
	ds_write_b128 v8, v[0:3] offset:64
	s_waitcnt lgkmcnt(0)
	s_barrier
	v_mbcnt_lo_u32_b32 v0, -1, 0
	v_mbcnt_hi_u32_b32 v0, -1, v0
	s_nop 0
	v_add_u32_e32 v0, s88, v0
	v_ashrrev_i32_e32 v12, 3, v0
	v_mbcnt_lo_u32_b32 v0, -1, 0
	v_mbcnt_hi_u32_b32 v0, -1, v0
	v_lshlrev_b32_e32 v1, 7, v12
	v_lshlrev_b32_e32 v0, 4, v0
	v_and_b32_e32 v13, 0x70, v0
	v_add3_u32 v4, s68, v1, v13
	ds_read_b128 v[0:3], v4
	ds_read_b128 v[4:7], v4 offset:8192
	global_load_dwordx4 v[8:11], v13, s[4:5]
	s_waitcnt lgkmcnt(0)
	v_pk_add_f32 v[0:1], v[0:1], v[4:5]
	v_mul_lo_u32 v4, v12, s70
	v_pk_add_f32 v[2:3], v[2:3], v[6:7]
	v_add3_u32 v4, s72, v4, v13
	v_mov_b32_e32 v5, 0
	v_mov_b32_e32 v6, 0
	v_mov_b32_e32 v7, 0
	s_waitcnt vmcnt(0)
	v_pk_add_f32 v[0:1], v[0:1], v[8:9]
	v_pk_add_f32 v[2:3], v[2:3], v[10:11]
	ds_write2_b32 v4, v0, v1 offset1:1
	ds_write2_b32 v4, v2, v3 offset0:2 offset1:3
	s_waitcnt lgkmcnt(0)
	s_barrier
	v_mbcnt_lo_u32_b32 v0, -1, 0
	v_mbcnt_hi_u32_b32 v0, -1, v0
	v_mov_b32_e32 v10, 0
	v_add_u32_e32 v0, s88, v0
	v_cmp_gt_i32_e32 vcc, 64, v0
	v_mov_b32_e32 v0, 0
	v_mov_b32_e32 v2, 0
	v_mov_b32_e32 v4, 0
	v_mov_b32_e32 v9, 0
	v_mov_b32_e32 v1, 0
	v_mov_b32_e32 v3, 0
	v_mov_b32_e32 v11, 0
	s_and_saveexec_b64 s[62:63], vcc
	s_cbranch_execz .LBB0_1503
	v_mbcnt_lo_u32_b32 v228, -1, 0
	v_mbcnt_hi_u32_b32 v228, -1, v228
	v_add_u32_e32 v228, s88, v228
	v_mul_lo_u32 v228, v228, s70
	v_add_u32_e32 v228, s72, v228
	ds_read_b32 v196, v228
	ds_read_b32 v197, v228 offset:4
	ds_read_b32 v198, v228 offset:8
	ds_read_b32 v199, v228 offset:12
	ds_read_b32 v200, v228 offset:16
	ds_read_b32 v201, v228 offset:20
	ds_read_b32 v202, v228 offset:24
	ds_read_b32 v203, v228 offset:28
	ds_read_b32 v204, v228 offset:32
	ds_read_b32 v205, v228 offset:36
	ds_read_b32 v206, v228 offset:40
	ds_read_b32 v207, v228 offset:44
	ds_read_b32 v208, v228 offset:48
	ds_read_b32 v209, v228 offset:52
	ds_read_b32 v210, v228 offset:56
	ds_read_b32 v211, v228 offset:60
	ds_read_b32 v212, v228 offset:64
	ds_read_b32 v213, v228 offset:68
	ds_read_b32 v214, v228 offset:72
	ds_read_b32 v215, v228 offset:76
	ds_read_b32 v216, v228 offset:80
	ds_read_b32 v217, v228 offset:84
	ds_read_b32 v218, v228 offset:88
	ds_read_b32 v219, v228 offset:92
	ds_read_b32 v220, v228 offset:96
	ds_read_b32 v221, v228 offset:100
	ds_read_b32 v222, v228 offset:104
	ds_read_b32 v223, v228 offset:108
	ds_read_b32 v224, v228 offset:112
	ds_read_b32 v225, v228 offset:116
	ds_read_b32 v226, v228 offset:120
	ds_read_b32 v227, v228 offset:124
	s_waitcnt lgkmcnt(0)
	v_mov_b32_e32 v229, v169
	v_mov_b32_e32 v32, 0
	v_cmp_gt_f32_e32 vcc, v196, v229
	s_nop 1
	v_cndmask_b32_e32 v229, v229, v196, vcc
	v_cndmask_b32_e64 v32, v32, 0, vcc
	v_cmp_gt_f32_e32 vcc, v197, v229
	s_nop 1
	v_cndmask_b32_e32 v229, v229, v197, vcc
	v_cndmask_b32_e64 v32, v32, 1, vcc
	v_cmp_gt_f32_e32 vcc, v198, v229
	s_nop 1
	v_cndmask_b32_e32 v229, v229, v198, vcc
	v_cndmask_b32_e64 v32, v32, 2, vcc
	v_cmp_gt_f32_e32 vcc, v199, v229
	s_nop 1
	v_cndmask_b32_e32 v229, v229, v199, vcc
	v_cndmask_b32_e64 v32, v32, 3, vcc
	v_cmp_gt_f32_e32 vcc, v200, v229
	s_nop 1
	v_cndmask_b32_e32 v229, v229, v200, vcc
	v_cndmask_b32_e64 v32, v32, 4, vcc
	v_cmp_gt_f32_e32 vcc, v201, v229
	s_nop 1
	v_cndmask_b32_e32 v229, v229, v201, vcc
	v_cndmask_b32_e64 v32, v32, 5, vcc
	v_cmp_gt_f32_e32 vcc, v202, v229
	s_nop 1
	v_cndmask_b32_e32 v229, v229, v202, vcc
	v_cndmask_b32_e64 v32, v32, 6, vcc
	v_cmp_gt_f32_e32 vcc, v203, v229
	s_nop 1
	v_cndmask_b32_e32 v229, v229, v203, vcc
	v_cndmask_b32_e64 v32, v32, 7, vcc
	v_cmp_gt_f32_e32 vcc, v204, v229
	s_nop 1
	v_cndmask_b32_e32 v229, v229, v204, vcc
	v_cndmask_b32_e64 v32, v32, 8, vcc
	v_cmp_gt_f32_e32 vcc, v205, v229
	s_nop 1
	v_cndmask_b32_e32 v229, v229, v205, vcc
	v_cndmask_b32_e64 v32, v32, 9, vcc
	v_cmp_gt_f32_e32 vcc, v206, v229
	s_nop 1
	v_cndmask_b32_e32 v229, v229, v206, vcc
	v_cndmask_b32_e64 v32, v32, 10, vcc
	v_cmp_gt_f32_e32 vcc, v207, v229
	s_nop 1
	v_cndmask_b32_e32 v229, v229, v207, vcc
	v_cndmask_b32_e64 v32, v32, 11, vcc
	v_cmp_gt_f32_e32 vcc, v208, v229
	s_nop 1
	v_cndmask_b32_e32 v229, v229, v208, vcc
	v_cndmask_b32_e64 v32, v32, 12, vcc
	v_cmp_gt_f32_e32 vcc, v209, v229
	s_nop 1
	v_cndmask_b32_e32 v229, v229, v209, vcc
	v_cndmask_b32_e64 v32, v32, 13, vcc
	v_cmp_gt_f32_e32 vcc, v210, v229
	s_nop 1
	v_cndmask_b32_e32 v229, v229, v210, vcc
	v_cndmask_b32_e64 v32, v32, 14, vcc
	v_cmp_gt_f32_e32 vcc, v211, v229
	s_nop 1
	v_cndmask_b32_e32 v229, v229, v211, vcc
	v_cndmask_b32_e64 v32, v32, 15, vcc
	v_cmp_gt_f32_e32 vcc, v212, v229
	s_nop 1
	v_cndmask_b32_e32 v229, v229, v212, vcc
	v_cndmask_b32_e64 v32, v32, 16, vcc
	v_cmp_gt_f32_e32 vcc, v213, v229
	s_nop 1
	v_cndmask_b32_e32 v229, v229, v213, vcc
	v_cndmask_b32_e64 v32, v32, 17, vcc
	v_cmp_gt_f32_e32 vcc, v214, v229
	s_nop 1
	v_cndmask_b32_e32 v229, v229, v214, vcc
	v_cndmask_b32_e64 v32, v32, 18, vcc
	v_cmp_gt_f32_e32 vcc, v215, v229
	s_nop 1
	v_cndmask_b32_e32 v229, v229, v215, vcc
	v_cndmask_b32_e64 v32, v32, 19, vcc
	v_cmp_gt_f32_e32 vcc, v216, v229
	s_nop 1
	v_cndmask_b32_e32 v229, v229, v216, vcc
	v_cndmask_b32_e64 v32, v32, 20, vcc
	v_cmp_gt_f32_e32 vcc, v217, v229
	s_nop 1
	v_cndmask_b32_e32 v229, v229, v217, vcc
	v_cndmask_b32_e64 v32, v32, 21, vcc
	v_cmp_gt_f32_e32 vcc, v218, v229
	s_nop 1
	v_cndmask_b32_e32 v229, v229, v218, vcc
; __device__ __forceinline__ void p6_router(Frame& F) {
;     ...
;             for (int k = 0; k < 4; ++k) { float best = -3.0e38f; int bi = 0;
;                 for (int e = 0; e < NE; ++e) { const float v = lg[FTID * 33 + e]; const bool ok = !((used >> e) & 1u) && (v > best); best = ok ? v : best; bi = ok ? e : bi; }
;                 used |= 1u << bi; ek[k] = bi; lv[k] = best; }
	v_cndmask_b32_e64 v32, v32, 22, vcc
	v_cmp_gt_f32_e32 vcc, v219, v229
	s_nop 1
	v_cndmask_b32_e32 v229, v229, v219, vcc
	v_cndmask_b32_e64 v32, v32, 23, vcc
	v_cmp_gt_f32_e32 vcc, v220, v229
	s_nop 1
	v_cndmask_b32_e32 v229, v229, v220, vcc
	v_cndmask_b32_e64 v32, v32, 24, vcc
	v_cmp_gt_f32_e32 vcc, v221, v229
	s_nop 1
	v_cndmask_b32_e32 v229, v229, v221, vcc
	v_cndmask_b32_e64 v32, v32, 25, vcc
	v_cmp_gt_f32_e32 vcc, v222, v229
	s_nop 1
	v_cndmask_b32_e32 v229, v229, v222, vcc
	v_cndmask_b32_e64 v32, v32, 26, vcc
	v_cmp_gt_f32_e32 vcc, v223, v229
	s_nop 1
	v_cndmask_b32_e32 v229, v229, v223, vcc
	v_cndmask_b32_e64 v32, v32, 27, vcc
	v_cmp_gt_f32_e32 vcc, v224, v229
	s_nop 1
	v_cndmask_b32_e32 v229, v229, v224, vcc
	v_cndmask_b32_e64 v32, v32, 28, vcc
	v_cmp_gt_f32_e32 vcc, v225, v229
	s_nop 1
	v_cndmask_b32_e32 v229, v229, v225, vcc
	v_cndmask_b32_e64 v32, v32, 29, vcc
	v_cmp_gt_f32_e32 vcc, v226, v229
	s_nop 1
	v_cndmask_b32_e32 v229, v229, v226, vcc
	v_cndmask_b32_e64 v32, v32, 30, vcc
	v_cmp_gt_f32_e32 vcc, v227, v229
	s_nop 1
	v_cndmask_b32_e32 v229, v229, v227, vcc
	v_cndmask_b32_e64 v32, v32, 31, vcc
	v_cmp_eq_u32_e32 vcc, 0, v32
	s_nop 1
	v_cndmask_b32_e32 v196, v196, v169, vcc
	v_cmp_eq_u32_e32 vcc, 1, v32
	s_nop 1
	v_cndmask_b32_e32 v197, v197, v169, vcc
	v_cmp_eq_u32_e32 vcc, 2, v32
	s_nop 1
	v_cndmask_b32_e32 v198, v198, v169, vcc
	v_cmp_eq_u32_e32 vcc, 3, v32
	s_nop 1
	v_cndmask_b32_e32 v199, v199, v169, vcc
	v_cmp_eq_u32_e32 vcc, 4, v32
	s_nop 1
	v_cndmask_b32_e32 v200, v200, v169, vcc
	v_cmp_eq_u32_e32 vcc, 5, v32
	s_nop 1
	v_cndmask_b32_e32 v201, v201, v169, vcc
	v_cmp_eq_u32_e32 vcc, 6, v32
	s_nop 1
	v_cndmask_b32_e32 v202, v202, v169, vcc
	v_cmp_eq_u32_e32 vcc, 7, v32
	s_nop 1
	v_cndmask_b32_e32 v203, v203, v169, vcc
	v_cmp_eq_u32_e32 vcc, 8, v32
	s_nop 1
	v_cndmask_b32_e32 v204, v204, v169, vcc
	v_cmp_eq_u32_e32 vcc, 9, v32
	s_nop 1
	v_cndmask_b32_e32 v205, v205, v169, vcc
	v_cmp_eq_u32_e32 vcc, 10, v32
	s_nop 1
	v_cndmask_b32_e32 v206, v206, v169, vcc
	v_cmp_eq_u32_e32 vcc, 11, v32
	s_nop 1
	v_cndmask_b32_e32 v207, v207, v169, vcc
	v_cmp_eq_u32_e32 vcc, 12, v32
	s_nop 1
	v_cndmask_b32_e32 v208, v208, v169, vcc
	v_cmp_eq_u32_e32 vcc, 13, v32
	s_nop 1
	v_cndmask_b32_e32 v209, v209, v169, vcc
	v_cmp_eq_u32_e32 vcc, 14, v32
	s_nop 1
	v_cndmask_b32_e32 v210, v210, v169, vcc
	v_cmp_eq_u32_e32 vcc, 15, v32
	s_nop 1
	v_cndmask_b32_e32 v211, v211, v169, vcc
	v_cmp_eq_u32_e32 vcc, 16, v32
	s_nop 1
	v_cndmask_b32_e32 v212, v212, v169, vcc
	v_cmp_eq_u32_e32 vcc, 17, v32
	s_nop 1
	v_cndmask_b32_e32 v213, v213, v169, vcc
	v_cmp_eq_u32_e32 vcc, 18, v32
	s_nop 1
	v_cndmask_b32_e32 v214, v214, v169, vcc
	v_cmp_eq_u32_e32 vcc, 19, v32
	s_nop 1
	v_cndmask_b32_e32 v215, v215, v169, vcc
	v_cmp_eq_u32_e32 vcc, 20, v32
	s_nop 1
	v_cndmask_b32_e32 v216, v216, v169, vcc
	v_cmp_eq_u32_e32 vcc, 21, v32
	s_nop 1
	v_cndmask_b32_e32 v217, v217, v169, vcc
	v_cmp_eq_u32_e32 vcc, 22, v32
	s_nop 1
	v_cndmask_b32_e32 v218, v218, v169, vcc
	v_cmp_eq_u32_e32 vcc, 23, v32
	s_nop 1
	v_cndmask_b32_e32 v219, v219, v169, vcc
	v_cmp_eq_u32_e32 vcc, 24, v32
	s_nop 1
	v_cndmask_b32_e32 v220, v220, v169, vcc
	v_cmp_eq_u32_e32 vcc, 25, v32
	s_nop 1
	v_cndmask_b32_e32 v221, v221, v169, vcc
	v_cmp_eq_u32_e32 vcc, 26, v32
	s_nop 1
	v_cndmask_b32_e32 v222, v222, v169, vcc
	v_cmp_eq_u32_e32 vcc, 27, v32
	s_nop 1
	v_cndmask_b32_e32 v223, v223, v169, vcc
	v_cmp_eq_u32_e32 vcc, 28, v32
	s_nop 1
	v_cndmask_b32_e32 v224, v224, v169, vcc
	v_cmp_eq_u32_e32 vcc, 29, v32
	s_nop 1
	v_cndmask_b32_e32 v225, v225, v169, vcc
	v_cmp_eq_u32_e32 vcc, 30, v32
	s_nop 1
	v_cndmask_b32_e32 v226, v226, v169, vcc
	v_cmp_eq_u32_e32 vcc, 31, v32
	s_nop 1
	v_cndmask_b32_e32 v227, v227, v169, vcc
	v_mov_b32_e32 v230, v169
	v_mov_b32_e32 v0, 0
	v_cmp_gt_f32_e32 vcc, v196, v230
	s_nop 1
	v_cndmask_b32_e32 v230, v230, v196, vcc
	v_cndmask_b32_e64 v0, v0, 0, vcc
	v_cmp_gt_f32_e32 vcc, v197, v230
	s_nop 1
	v_cndmask_b32_e32 v230, v230, v197, vcc
	v_cndmask_b32_e64 v0, v0, 1, vcc
	v_cmp_gt_f32_e32 vcc, v198, v230
	s_nop 1
	v_cndmask_b32_e32 v230, v230, v198, vcc
	v_cndmask_b32_e64 v0, v0, 2, vcc
	v_cmp_gt_f32_e32 vcc, v199, v230
	s_nop 1
	v_cndmask_b32_e32 v230, v230, v199, vcc
	v_cndmask_b32_e64 v0, v0, 3, vcc
	v_cmp_gt_f32_e32 vcc, v200, v230
	s_nop 1
	v_cndmask_b32_e32 v230, v230, v200, vcc
	v_cndmask_b32_e64 v0, v0, 4, vcc
	v_cmp_gt_f32_e32 vcc, v201, v230
	s_nop 1
	v_cndmask_b32_e32 v230, v230, v201, vcc
	v_cndmask_b32_e64 v0, v0, 5, vcc
	v_cmp_gt_f32_e32 vcc, v202, v230
	s_nop 1
	v_cndmask_b32_e32 v230, v230, v202, vcc
	v_cndmask_b32_e64 v0, v0, 6, vcc
	v_cmp_gt_f32_e32 vcc, v203, v230
	s_nop 1
	v_cndmask_b32_e32 v230, v230, v203, vcc
	v_cndmask_b32_e64 v0, v0, 7, vcc
	v_cmp_gt_f32_e32 vcc, v204, v230
	s_nop 1
	v_cndmask_b32_e32 v230, v230, v204, vcc
	v_cndmask_b32_e64 v0, v0, 8, vcc
	v_cmp_gt_f32_e32 vcc, v205, v230
	s_nop 1
	v_cndmask_b32_e32 v230, v230, v205, vcc
	v_cndmask_b32_e64 v0, v0, 9, vcc
	v_cmp_gt_f32_e32 vcc, v206, v230
	s_nop 1
	v_cndmask_b32_e32 v230, v230, v206, vcc
	v_cndmask_b32_e64 v0, v0, 10, vcc
	v_cmp_gt_f32_e32 vcc, v207, v230
	s_nop 1
	v_cndmask_b32_e32 v230, v230, v207, vcc
	v_cndmask_b32_e64 v0, v0, 11, vcc
	v_cmp_gt_f32_e32 vcc, v208, v230
	s_nop 1
	v_cndmask_b32_e32 v230, v230, v208, vcc
	v_cndmask_b32_e64 v0, v0, 12, vcc
	v_cmp_gt_f32_e32 vcc, v209, v230
	s_nop 1
	v_cndmask_b32_e32 v230, v230, v209, vcc
	v_cndmask_b32_e64 v0, v0, 13, vcc
	v_cmp_gt_f32_e32 vcc, v210, v230
	s_nop 1
	v_cndmask_b32_e32 v230, v230, v210, vcc
	v_cndmask_b32_e64 v0, v0, 14, vcc
	v_cmp_gt_f32_e32 vcc, v211, v230
	s_nop 1
	v_cndmask_b32_e32 v230, v230, v211, vcc
	v_cndmask_b32_e64 v0, v0, 15, vcc
; __device__ __forceinline__ void p6_router(Frame& F) {
;     ...
;         int ek[4] = {0, 0, 0, 0}, lp[4] = {0, 0, 0, 0}; float gk[4] = {0.f, 0.f, 0.f, 0.f};
;         if (FTID < 64) {
;             float lv[4]; unsigned used = 0u;
; #pragma unroll
;             for (int k = 0; k < 4; ++k) { float best = -3.0e38f; int bi = 0;
;                 for (int e = 0; e < NE; ++e) { const float v = lg[FTID * 33 + e]; const bool ok = !((used >> e) & 1u) && (v > best); best = ok ? v : best; bi = ok ? e : bi; }
;                 used |= 1u << bi; ek[k] = bi; lv[k] = best; }
	v_cmp_gt_f32_e32 vcc, v212, v230
	s_nop 1
	v_cndmask_b32_e32 v230, v230, v212, vcc
	v_cndmask_b32_e64 v0, v0, 16, vcc
	v_cmp_gt_f32_e32 vcc, v213, v230
	s_nop 1
	v_cndmask_b32_e32 v230, v230, v213, vcc
	v_cndmask_b32_e64 v0, v0, 17, vcc
	v_cmp_gt_f32_e32 vcc, v214, v230
	s_nop 1
	v_cndmask_b32_e32 v230, v230, v214, vcc
	v_cndmask_b32_e64 v0, v0, 18, vcc
	v_cmp_gt_f32_e32 vcc, v215, v230
	s_nop 1
	v_cndmask_b32_e32 v230, v230, v215, vcc
	v_cndmask_b32_e64 v0, v0, 19, vcc
	v_cmp_gt_f32_e32 vcc, v216, v230
	s_nop 1
	v_cndmask_b32_e32 v230, v230, v216, vcc
	v_cndmask_b32_e64 v0, v0, 20, vcc
	v_cmp_gt_f32_e32 vcc, v217, v230
	s_nop 1
	v_cndmask_b32_e32 v230, v230, v217, vcc
	v_cndmask_b32_e64 v0, v0, 21, vcc
	v_cmp_gt_f32_e32 vcc, v218, v230
	s_nop 1
	v_cndmask_b32_e32 v230, v230, v218, vcc
	v_cndmask_b32_e64 v0, v0, 22, vcc
	v_cmp_gt_f32_e32 vcc, v219, v230
	s_nop 1
	v_cndmask_b32_e32 v230, v230, v219, vcc
	v_cndmask_b32_e64 v0, v0, 23, vcc
	v_cmp_gt_f32_e32 vcc, v220, v230
	s_nop 1
	v_cndmask_b32_e32 v230, v230, v220, vcc
	v_cndmask_b32_e64 v0, v0, 24, vcc
	v_cmp_gt_f32_e32 vcc, v221, v230
	s_nop 1
	v_cndmask_b32_e32 v230, v230, v221, vcc
	v_cndmask_b32_e64 v0, v0, 25, vcc
	v_cmp_gt_f32_e32 vcc, v222, v230
	s_nop 1
	v_cndmask_b32_e32 v230, v230, v222, vcc
	v_cndmask_b32_e64 v0, v0, 26, vcc
	v_cmp_gt_f32_e32 vcc, v223, v230
	s_nop 1
	v_cndmask_b32_e32 v230, v230, v223, vcc
	v_cndmask_b32_e64 v0, v0, 27, vcc
	v_cmp_gt_f32_e32 vcc, v224, v230
	s_nop 1
	v_cndmask_b32_e32 v230, v230, v224, vcc
	v_cndmask_b32_e64 v0, v0, 28, vcc
	v_cmp_gt_f32_e32 vcc, v225, v230
	s_nop 1
	v_cndmask_b32_e32 v230, v230, v225, vcc
	v_cndmask_b32_e64 v0, v0, 29, vcc
	v_cmp_gt_f32_e32 vcc, v226, v230
	s_nop 1
	v_cndmask_b32_e32 v230, v230, v226, vcc
	v_cndmask_b32_e64 v0, v0, 30, vcc
	v_cmp_gt_f32_e32 vcc, v227, v230
	s_nop 1
	v_cndmask_b32_e32 v230, v230, v227, vcc
	v_cndmask_b32_e64 v0, v0, 31, vcc
	v_cmp_eq_u32_e32 vcc, 0, v0
	s_nop 1
	v_cndmask_b32_e32 v196, v196, v169, vcc
	v_cmp_eq_u32_e32 vcc, 1, v0
	s_nop 1
	v_cndmask_b32_e32 v197, v197, v169, vcc
	v_cmp_eq_u32_e32 vcc, 2, v0
	s_nop 1
	v_cndmask_b32_e32 v198, v198, v169, vcc
	v_cmp_eq_u32_e32 vcc, 3, v0
	s_nop 1
	v_cndmask_b32_e32 v199, v199, v169, vcc
	v_cmp_eq_u32_e32 vcc, 4, v0
	s_nop 1
	v_cndmask_b32_e32 v200, v200, v169, vcc
	v_cmp_eq_u32_e32 vcc, 5, v0
	s_nop 1
	v_cndmask_b32_e32 v201, v201, v169, vcc
	v_cmp_eq_u32_e32 vcc, 6, v0
	s_nop 1
	v_cndmask_b32_e32 v202, v202, v169, vcc
	v_cmp_eq_u32_e32 vcc, 7, v0
	s_nop 1
	v_cndmask_b32_e32 v203, v203, v169, vcc
	v_cmp_eq_u32_e32 vcc, 8, v0
	s_nop 1
	v_cndmask_b32_e32 v204, v204, v169, vcc
	v_cmp_eq_u32_e32 vcc, 9, v0
	s_nop 1
	v_cndmask_b32_e32 v205, v205, v169, vcc
	v_cmp_eq_u32_e32 vcc, 10, v0
	s_nop 1
	v_cndmask_b32_e32 v206, v206, v169, vcc
	v_cmp_eq_u32_e32 vcc, 11, v0
	s_nop 1
	v_cndmask_b32_e32 v207, v207, v169, vcc
	v_cmp_eq_u32_e32 vcc, 12, v0
	s_nop 1
	v_cndmask_b32_e32 v208, v208, v169, vcc
	v_cmp_eq_u32_e32 vcc, 13, v0
	s_nop 1
	v_cndmask_b32_e32 v209, v209, v169, vcc
	v_cmp_eq_u32_e32 vcc, 14, v0
	s_nop 1
	v_cndmask_b32_e32 v210, v210, v169, vcc
	v_cmp_eq_u32_e32 vcc, 15, v0
	s_nop 1
	v_cndmask_b32_e32 v211, v211, v169, vcc
	v_cmp_eq_u32_e32 vcc, 16, v0
	s_nop 1
	v_cndmask_b32_e32 v212, v212, v169, vcc
	v_cmp_eq_u32_e32 vcc, 17, v0
	s_nop 1
	v_cndmask_b32_e32 v213, v213, v169, vcc
	v_cmp_eq_u32_e32 vcc, 18, v0
	s_nop 1
	v_cndmask_b32_e32 v214, v214, v169, vcc
	v_cmp_eq_u32_e32 vcc, 19, v0
	s_nop 1
	v_cndmask_b32_e32 v215, v215, v169, vcc
	v_cmp_eq_u32_e32 vcc, 20, v0
	s_nop 1
	v_cndmask_b32_e32 v216, v216, v169, vcc
	v_cmp_eq_u32_e32 vcc, 21, v0
	s_nop 1
	v_cndmask_b32_e32 v217, v217, v169, vcc
	v_cmp_eq_u32_e32 vcc, 22, v0
	s_nop 1
	v_cndmask_b32_e32 v218, v218, v169, vcc
	v_cmp_eq_u32_e32 vcc, 23, v0
	s_nop 1
	v_cndmask_b32_e32 v219, v219, v169, vcc
	v_cmp_eq_u32_e32 vcc, 24, v0
	s_nop 1
	v_cndmask_b32_e32 v220, v220, v169, vcc
	v_cmp_eq_u32_e32 vcc, 25, v0
	s_nop 1
	v_cndmask_b32_e32 v221, v221, v169, vcc
	v_cmp_eq_u32_e32 vcc, 26, v0
	s_nop 1
	v_cndmask_b32_e32 v222, v222, v169, vcc
	v_cmp_eq_u32_e32 vcc, 27, v0
	s_nop 1
	v_cndmask_b32_e32 v223, v223, v169, vcc
	v_cmp_eq_u32_e32 vcc, 28, v0
	s_nop 1
	v_cndmask_b32_e32 v224, v224, v169, vcc
	v_cmp_eq_u32_e32 vcc, 29, v0
	s_nop 1
	v_cndmask_b32_e32 v225, v225, v169, vcc
	v_cmp_eq_u32_e32 vcc, 30, v0
	s_nop 1
	v_cndmask_b32_e32 v226, v226, v169, vcc
	v_cmp_eq_u32_e32 vcc, 31, v0
	s_nop 1
	v_cndmask_b32_e32 v227, v227, v169, vcc
	v_mov_b32_e32 v231, v169
	v_mov_b32_e32 v2, 0
	v_cmp_gt_f32_e32 vcc, v196, v231
	s_nop 1
	v_cndmask_b32_e32 v231, v231, v196, vcc
	v_cndmask_b32_e64 v2, v2, 0, vcc
	v_cmp_gt_f32_e32 vcc, v197, v231
	s_nop 1
	v_cndmask_b32_e32 v231, v231, v197, vcc
	v_cndmask_b32_e64 v2, v2, 1, vcc
	v_cmp_gt_f32_e32 vcc, v198, v231
	s_nop 1
	v_cndmask_b32_e32 v231, v231, v198, vcc
	v_cndmask_b32_e64 v2, v2, 2, vcc
	v_cmp_gt_f32_e32 vcc, v199, v231
	s_nop 1
	v_cndmask_b32_e32 v231, v231, v199, vcc
	v_cndmask_b32_e64 v2, v2, 3, vcc
	v_cmp_gt_f32_e32 vcc, v200, v231
	s_nop 1
	v_cndmask_b32_e32 v231, v231, v200, vcc
	v_cndmask_b32_e64 v2, v2, 4, vcc
	v_cmp_gt_f32_e32 vcc, v201, v231
	s_nop 1
	v_cndmask_b32_e32 v231, v231, v201, vcc
	v_cndmask_b32_e64 v2, v2, 5, vcc
	v_cmp_gt_f32_e32 vcc, v202, v231
	s_nop 1
	v_cndmask_b32_e32 v231, v231, v202, vcc
	v_cndmask_b32_e64 v2, v2, 6, vcc
	v_cmp_gt_f32_e32 vcc, v203, v231
	s_nop 1
	v_cndmask_b32_e32 v231, v231, v203, vcc
	v_cndmask_b32_e64 v2, v2, 7, vcc
	v_cmp_gt_f32_e32 vcc, v204, v231
	s_nop 1
	v_cndmask_b32_e32 v231, v231, v204, vcc
	v_cndmask_b32_e64 v2, v2, 8, vcc
	v_cmp_gt_f32_e32 vcc, v205, v231
	s_nop 1
	v_cndmask_b32_e32 v231, v231, v205, vcc
; __device__ __forceinline__ void p6_router(Frame& F) {
;     ...
;             for (int k = 0; k < 4; ++k) { float best = -3.0e38f; int bi = 0;
;                 for (int e = 0; e < NE; ++e) { const float v = lg[FTID * 33 + e]; const bool ok = !((used >> e) & 1u) && (v > best); best = ok ? v : best; bi = ok ? e : bi; }
;                 used |= 1u << bi; ek[k] = bi; lv[k] = best; }
	v_cndmask_b32_e64 v2, v2, 9, vcc
	v_cmp_gt_f32_e32 vcc, v206, v231
	s_nop 1
	v_cndmask_b32_e32 v231, v231, v206, vcc
	v_cndmask_b32_e64 v2, v2, 10, vcc
	v_cmp_gt_f32_e32 vcc, v207, v231
	s_nop 1
	v_cndmask_b32_e32 v231, v231, v207, vcc
	v_cndmask_b32_e64 v2, v2, 11, vcc
	v_cmp_gt_f32_e32 vcc, v208, v231
	s_nop 1
	v_cndmask_b32_e32 v231, v231, v208, vcc
	v_cndmask_b32_e64 v2, v2, 12, vcc
	v_cmp_gt_f32_e32 vcc, v209, v231
	s_nop 1
	v_cndmask_b32_e32 v231, v231, v209, vcc
	v_cndmask_b32_e64 v2, v2, 13, vcc
	v_cmp_gt_f32_e32 vcc, v210, v231
	s_nop 1
	v_cndmask_b32_e32 v231, v231, v210, vcc
	v_cndmask_b32_e64 v2, v2, 14, vcc
	v_cmp_gt_f32_e32 vcc, v211, v231
	s_nop 1
	v_cndmask_b32_e32 v231, v231, v211, vcc
	v_cndmask_b32_e64 v2, v2, 15, vcc
	v_cmp_gt_f32_e32 vcc, v212, v231
	s_nop 1
	v_cndmask_b32_e32 v231, v231, v212, vcc
	v_cndmask_b32_e64 v2, v2, 16, vcc
	v_cmp_gt_f32_e32 vcc, v213, v231
	s_nop 1
	v_cndmask_b32_e32 v231, v231, v213, vcc
	v_cndmask_b32_e64 v2, v2, 17, vcc
	v_cmp_gt_f32_e32 vcc, v214, v231
	s_nop 1
	v_cndmask_b32_e32 v231, v231, v214, vcc
	v_cndmask_b32_e64 v2, v2, 18, vcc
	v_cmp_gt_f32_e32 vcc, v215, v231
	s_nop 1
	v_cndmask_b32_e32 v231, v231, v215, vcc
	v_cndmask_b32_e64 v2, v2, 19, vcc
	v_cmp_gt_f32_e32 vcc, v216, v231
	s_nop 1
	v_cndmask_b32_e32 v231, v231, v216, vcc
	v_cndmask_b32_e64 v2, v2, 20, vcc
	v_cmp_gt_f32_e32 vcc, v217, v231
	s_nop 1
	v_cndmask_b32_e32 v231, v231, v217, vcc
	v_cndmask_b32_e64 v2, v2, 21, vcc
	v_cmp_gt_f32_e32 vcc, v218, v231
	s_nop 1
	v_cndmask_b32_e32 v231, v231, v218, vcc
	v_cndmask_b32_e64 v2, v2, 22, vcc
	v_cmp_gt_f32_e32 vcc, v219, v231
	s_nop 1
	v_cndmask_b32_e32 v231, v231, v219, vcc
	v_cndmask_b32_e64 v2, v2, 23, vcc
	v_cmp_gt_f32_e32 vcc, v220, v231
	s_nop 1
	v_cndmask_b32_e32 v231, v231, v220, vcc
	v_cndmask_b32_e64 v2, v2, 24, vcc
	v_cmp_gt_f32_e32 vcc, v221, v231
	s_nop 1
	v_cndmask_b32_e32 v231, v231, v221, vcc
	v_cndmask_b32_e64 v2, v2, 25, vcc
	v_cmp_gt_f32_e32 vcc, v222, v231
	s_nop 1
	v_cndmask_b32_e32 v231, v231, v222, vcc
	v_cndmask_b32_e64 v2, v2, 26, vcc
	v_cmp_gt_f32_e32 vcc, v223, v231
	s_nop 1
	v_cndmask_b32_e32 v231, v231, v223, vcc
	v_cndmask_b32_e64 v2, v2, 27, vcc
	v_cmp_gt_f32_e32 vcc, v224, v231
	s_nop 1
	v_cndmask_b32_e32 v231, v231, v224, vcc
	v_cndmask_b32_e64 v2, v2, 28, vcc
	v_cmp_gt_f32_e32 vcc, v225, v231
	s_nop 1
	v_cndmask_b32_e32 v231, v231, v225, vcc
	v_cndmask_b32_e64 v2, v2, 29, vcc
	v_cmp_gt_f32_e32 vcc, v226, v231
	s_nop 1
	v_cndmask_b32_e32 v231, v231, v226, vcc
	v_cndmask_b32_e64 v2, v2, 30, vcc
	v_cmp_gt_f32_e32 vcc, v227, v231
	s_nop 1
	v_cndmask_b32_e32 v231, v231, v227, vcc
	v_cndmask_b32_e64 v2, v2, 31, vcc
	v_cmp_eq_u32_e32 vcc, 0, v2
	s_nop 1
	v_cndmask_b32_e32 v196, v196, v169, vcc
	v_cmp_eq_u32_e32 vcc, 1, v2
	s_nop 1
	v_cndmask_b32_e32 v197, v197, v169, vcc
	v_cmp_eq_u32_e32 vcc, 2, v2
	s_nop 1
	v_cndmask_b32_e32 v198, v198, v169, vcc
	v_cmp_eq_u32_e32 vcc, 3, v2
	s_nop 1
	v_cndmask_b32_e32 v199, v199, v169, vcc
	v_cmp_eq_u32_e32 vcc, 4, v2
	s_nop 1
	v_cndmask_b32_e32 v200, v200, v169, vcc
	v_cmp_eq_u32_e32 vcc, 5, v2
	s_nop 1
	v_cndmask_b32_e32 v201, v201, v169, vcc
	v_cmp_eq_u32_e32 vcc, 6, v2
	s_nop 1
	v_cndmask_b32_e32 v202, v202, v169, vcc
	v_cmp_eq_u32_e32 vcc, 7, v2
	s_nop 1
	v_cndmask_b32_e32 v203, v203, v169, vcc
	v_cmp_eq_u32_e32 vcc, 8, v2
	s_nop 1
	v_cndmask_b32_e32 v204, v204, v169, vcc
	v_cmp_eq_u32_e32 vcc, 9, v2
	s_nop 1
	v_cndmask_b32_e32 v205, v205, v169, vcc
	v_cmp_eq_u32_e32 vcc, 10, v2
	s_nop 1
	v_cndmask_b32_e32 v206, v206, v169, vcc
	v_cmp_eq_u32_e32 vcc, 11, v2
	s_nop 1
	v_cndmask_b32_e32 v207, v207, v169, vcc
	v_cmp_eq_u32_e32 vcc, 12, v2
	s_nop 1
	v_cndmask_b32_e32 v208, v208, v169, vcc
	v_cmp_eq_u32_e32 vcc, 13, v2
	s_nop 1
	v_cndmask_b32_e32 v209, v209, v169, vcc
	v_cmp_eq_u32_e32 vcc, 14, v2
	s_nop 1
	v_cndmask_b32_e32 v210, v210, v169, vcc
	v_cmp_eq_u32_e32 vcc, 15, v2
	s_nop 1
	v_cndmask_b32_e32 v211, v211, v169, vcc
	v_cmp_eq_u32_e32 vcc, 16, v2
	s_nop 1
	v_cndmask_b32_e32 v212, v212, v169, vcc
	v_cmp_eq_u32_e32 vcc, 17, v2
	s_nop 1
	v_cndmask_b32_e32 v213, v213, v169, vcc
	v_cmp_eq_u32_e32 vcc, 18, v2
	s_nop 1
	v_cndmask_b32_e32 v214, v214, v169, vcc
	v_cmp_eq_u32_e32 vcc, 19, v2
	s_nop 1
	v_cndmask_b32_e32 v215, v215, v169, vcc
	v_cmp_eq_u32_e32 vcc, 20, v2
	s_nop 1
	v_cndmask_b32_e32 v216, v216, v169, vcc
	v_cmp_eq_u32_e32 vcc, 21, v2
	s_nop 1
	v_cndmask_b32_e32 v217, v217, v169, vcc
	v_cmp_eq_u32_e32 vcc, 22, v2
	s_nop 1
	v_cndmask_b32_e32 v218, v218, v169, vcc
	v_cmp_eq_u32_e32 vcc, 23, v2
	s_nop 1
	v_cndmask_b32_e32 v219, v219, v169, vcc
	v_cmp_eq_u32_e32 vcc, 24, v2
	s_nop 1
	v_cndmask_b32_e32 v220, v220, v169, vcc
	v_cmp_eq_u32_e32 vcc, 25, v2
	s_nop 1
	v_cndmask_b32_e32 v221, v221, v169, vcc
	v_cmp_eq_u32_e32 vcc, 26, v2
	s_nop 1
	v_cndmask_b32_e32 v222, v222, v169, vcc
	v_cmp_eq_u32_e32 vcc, 27, v2
	s_nop 1
	v_cndmask_b32_e32 v223, v223, v169, vcc
	v_cmp_eq_u32_e32 vcc, 28, v2
	s_nop 1
	v_cndmask_b32_e32 v224, v224, v169, vcc
	v_cmp_eq_u32_e32 vcc, 29, v2
	s_nop 1
	v_cndmask_b32_e32 v225, v225, v169, vcc
	v_cmp_eq_u32_e32 vcc, 30, v2
	s_nop 1
	v_cndmask_b32_e32 v226, v226, v169, vcc
	v_cmp_eq_u32_e32 vcc, 31, v2
; __device__ __forceinline__ float fexp(float x) { return __builtin_amdgcn_exp2f(x * 1.4426950408889634f); }
; __device__ __forceinline__ void p6_router(Frame& F) {
;     ...
;             for (int k = 0; k < 4; ++k) { float best = -3.0e38f; int bi = 0;
;                 for (int e = 0; e < NE; ++e) { const float v = lg[FTID * 33 + e]; const bool ok = !((used >> e) & 1u) && (v > best); best = ok ? v : best; bi = ok ? e : bi; }
;                 used |= 1u << bi; ek[k] = bi; lv[k] = best; }
;             const float mx = lv[0]; float den = 0.f;
; #pragma unroll
;             for (int k = 0; k < 4; ++k) { gk[k] = fexp(lv[k] - mx); den += gk[k]; }
;             const float rd = 1.f / den;
; #pragma unroll
;             for (int k = 0; k < 4; ++k) { gk[k] *= rd; lp[k] = __hip_atomic_fetch_add(&hist[ek[k]], 1, __ATOMIC_RELAXED, __HIP_MEMORY_SCOPE_WORKGROUP); }
	s_nop 1
	v_cndmask_b32_e32 v227, v227, v169, vcc
	v_mov_b32_e32 v232, v169
	v_mov_b32_e32 v4, 0
	v_cmp_gt_f32_e32 vcc, v196, v232
	s_nop 1
	v_cndmask_b32_e32 v232, v232, v196, vcc
	v_cndmask_b32_e64 v4, v4, 0, vcc
	v_cmp_gt_f32_e32 vcc, v197, v232
	s_nop 1
	v_cndmask_b32_e32 v232, v232, v197, vcc
	v_cndmask_b32_e64 v4, v4, 1, vcc
	v_cmp_gt_f32_e32 vcc, v198, v232
	s_nop 1
	v_cndmask_b32_e32 v232, v232, v198, vcc
	v_cndmask_b32_e64 v4, v4, 2, vcc
	v_cmp_gt_f32_e32 vcc, v199, v232
	s_nop 1
	v_cndmask_b32_e32 v232, v232, v199, vcc
	v_cndmask_b32_e64 v4, v4, 3, vcc
	v_cmp_gt_f32_e32 vcc, v200, v232
	s_nop 1
	v_cndmask_b32_e32 v232, v232, v200, vcc
	v_cndmask_b32_e64 v4, v4, 4, vcc
	v_cmp_gt_f32_e32 vcc, v201, v232
	s_nop 1
	v_cndmask_b32_e32 v232, v232, v201, vcc
	v_cndmask_b32_e64 v4, v4, 5, vcc
	v_cmp_gt_f32_e32 vcc, v202, v232
	s_nop 1
	v_cndmask_b32_e32 v232, v232, v202, vcc
	v_cndmask_b32_e64 v4, v4, 6, vcc
	v_cmp_gt_f32_e32 vcc, v203, v232
	s_nop 1
	v_cndmask_b32_e32 v232, v232, v203, vcc
	v_cndmask_b32_e64 v4, v4, 7, vcc
	v_cmp_gt_f32_e32 vcc, v204, v232
	s_nop 1
	v_cndmask_b32_e32 v232, v232, v204, vcc
	v_cndmask_b32_e64 v4, v4, 8, vcc
	v_cmp_gt_f32_e32 vcc, v205, v232
	s_nop 1
	v_cndmask_b32_e32 v232, v232, v205, vcc
	v_cndmask_b32_e64 v4, v4, 9, vcc
	v_cmp_gt_f32_e32 vcc, v206, v232
	s_nop 1
	v_cndmask_b32_e32 v232, v232, v206, vcc
	v_cndmask_b32_e64 v4, v4, 10, vcc
	v_cmp_gt_f32_e32 vcc, v207, v232
	s_nop 1
	v_cndmask_b32_e32 v232, v232, v207, vcc
	v_cndmask_b32_e64 v4, v4, 11, vcc
	v_cmp_gt_f32_e32 vcc, v208, v232
	s_nop 1
	v_cndmask_b32_e32 v232, v232, v208, vcc
	v_cndmask_b32_e64 v4, v4, 12, vcc
	v_cmp_gt_f32_e32 vcc, v209, v232
	s_nop 1
	v_cndmask_b32_e32 v232, v232, v209, vcc
	v_cndmask_b32_e64 v4, v4, 13, vcc
	v_cmp_gt_f32_e32 vcc, v210, v232
	s_nop 1
	v_cndmask_b32_e32 v232, v232, v210, vcc
	v_cndmask_b32_e64 v4, v4, 14, vcc
	v_cmp_gt_f32_e32 vcc, v211, v232
	s_nop 1
	v_cndmask_b32_e32 v232, v232, v211, vcc
	v_cndmask_b32_e64 v4, v4, 15, vcc
	v_cmp_gt_f32_e32 vcc, v212, v232
	s_nop 1
	v_cndmask_b32_e32 v232, v232, v212, vcc
	v_cndmask_b32_e64 v4, v4, 16, vcc
	v_cmp_gt_f32_e32 vcc, v213, v232
	s_nop 1
	v_cndmask_b32_e32 v232, v232, v213, vcc
	v_cndmask_b32_e64 v4, v4, 17, vcc
	v_cmp_gt_f32_e32 vcc, v214, v232
	s_nop 1
	v_cndmask_b32_e32 v232, v232, v214, vcc
	v_cndmask_b32_e64 v4, v4, 18, vcc
	v_cmp_gt_f32_e32 vcc, v215, v232
	s_nop 1
	v_cndmask_b32_e32 v232, v232, v215, vcc
	v_cndmask_b32_e64 v4, v4, 19, vcc
	v_cmp_gt_f32_e32 vcc, v216, v232
	s_nop 1
	v_cndmask_b32_e32 v232, v232, v216, vcc
	v_cndmask_b32_e64 v4, v4, 20, vcc
	v_cmp_gt_f32_e32 vcc, v217, v232
	s_nop 1
	v_cndmask_b32_e32 v232, v232, v217, vcc
	v_cndmask_b32_e64 v4, v4, 21, vcc
	v_cmp_gt_f32_e32 vcc, v218, v232
	s_nop 1
	v_cndmask_b32_e32 v232, v232, v218, vcc
	v_cndmask_b32_e64 v4, v4, 22, vcc
	v_cmp_gt_f32_e32 vcc, v219, v232
	s_nop 1
	v_cndmask_b32_e32 v232, v232, v219, vcc
	v_cndmask_b32_e64 v4, v4, 23, vcc
	v_cmp_gt_f32_e32 vcc, v220, v232
	s_nop 1
	v_cndmask_b32_e32 v232, v232, v220, vcc
	v_cndmask_b32_e64 v4, v4, 24, vcc
	v_cmp_gt_f32_e32 vcc, v221, v232
	s_nop 1
	v_cndmask_b32_e32 v232, v232, v221, vcc
	v_cndmask_b32_e64 v4, v4, 25, vcc
	v_cmp_gt_f32_e32 vcc, v222, v232
	s_nop 1
	v_cndmask_b32_e32 v232, v232, v222, vcc
	v_cndmask_b32_e64 v4, v4, 26, vcc
	v_cmp_gt_f32_e32 vcc, v223, v232
	s_nop 1
	v_cndmask_b32_e32 v232, v232, v223, vcc
	v_cndmask_b32_e64 v4, v4, 27, vcc
	v_cmp_gt_f32_e32 vcc, v224, v232
	s_nop 1
	v_cndmask_b32_e32 v232, v232, v224, vcc
	v_cndmask_b32_e64 v4, v4, 28, vcc
	v_cmp_gt_f32_e32 vcc, v225, v232
	s_nop 1
	v_cndmask_b32_e32 v232, v232, v225, vcc
	v_cndmask_b32_e64 v4, v4, 29, vcc
	v_cmp_gt_f32_e32 vcc, v226, v232
	s_nop 1
	v_cndmask_b32_e32 v232, v232, v226, vcc
	v_cndmask_b32_e64 v4, v4, 30, vcc
	v_cmp_gt_f32_e32 vcc, v227, v232
	s_nop 1
	v_cndmask_b32_e32 v232, v232, v227, vcc
	v_cndmask_b32_e64 v4, v4, 31, vcc
	v_sub_f32_e32 v233, v229, v229
	v_mul_f32_e32 v233, 0x3fb8aa3b, v233
	v_exp_f32_e32 v10, v233
	v_sub_f32_e32 v233, v230, v229
	v_mul_f32_e32 v233, 0x3fb8aa3b, v233
	v_exp_f32_e32 v11, v233
	v_sub_f32_e32 v233, v231, v229
	v_mul_f32_e32 v233, 0x3fb8aa3b, v233
	v_exp_f32_e32 v6, v233
	v_sub_f32_e32 v233, v232, v229
	v_mul_f32_e32 v233, 0x3fb8aa3b, v233
	v_exp_f32_e32 v7, v233
	s_nop 0
	v_add_f32_e32 v233, 0, v10
	v_add_f32_e32 v233, v233, v11
	v_add_f32_e32 v233, v233, v6
	v_add_f32_e32 v1, v233, v7
	v_div_scale_f32 v3, s[4:5], v1, v1, 1.0
	v_rcp_f32_e32 v5, v3
	s_nop 0
	v_fma_f32 v8, -v3, v5, 1.0
	v_fmac_f32_e32 v5, v8, v5
	v_div_scale_f32 v8, vcc, 1.0, v1, 1.0
	v_mul_f32_e32 v9, v8, v5
	v_fma_f32 v12, -v3, v9, v8
	v_fmac_f32_e32 v9, v12, v5
	v_fma_f32 v3, -v3, v9, v8
	v_div_fmas_f32 v3, v3, v5, v9
	v_div_fixup_f32 v234, v3, v1, 1.0
	s_add_i32 s0, 0, 0x1af00
	v_lshl_add_u32 v235, v32, 2, s0
	ds_add_rtn_u32 v9, v235, v168
	v_lshl_add_u32 v235, v0, 2, s0
	ds_add_rtn_u32 v1, v235, v168
	v_lshl_add_u32 v235, v2, 2, s0
	ds_add_rtn_u32 v3, v235, v168
	v_lshl_add_u32 v235, v4, 2, s0
	ds_add_rtn_u32 v5, v235, v168
	v_pk_mul_f32 v[10:11], v[10:11], v[234:235] op_sel_hi:[1,0]
	v_pk_mul_f32 v[6:7], v[6:7], v[234:235] op_sel_hi:[1,0]
